# speedup vs baseline: 1.0055x; 1.0055x over previous
.LBB5_140:
	v_lshl_or_b32 v2, s42, 3, v187
	v_ashrrev_i32_e32 v3, 31, v2
	v_lshlrev_b64 v[2:3], 16, v[2:3]
	v_lshl_add_u64 v[2:3], s[48:49], 0, v[2:3]
	v_mov_b32_e32 v169, 0
	v_lshlrev_b32_e32 v168, 4, v189
	s_or_b32 s25, s2, s50
	s_or_b32 s24, s50, 1
	s_mov_b32 s1, 0
	v_lshl_add_u64 v[166:167], v[2:3], 0, v[168:169]
	s_lshl_b32 s0, s25, 12
	s_or_b32 s30, s2, s24
	v_lshl_add_u64 v[18:19], v[166:167], 0, s[0:1]
	s_lshl_b32 s0, s30, 12
	v_lshl_add_u64 v[34:35], v[166:167], 0, s[0:1]
	global_load_dwordx4 v[2:5], v[18:19], off
	global_load_dwordx4 v[6:9], v[18:19], off offset:1024
	global_load_dwordx4 v[10:13], v[18:19], off offset:2048
	global_load_dwordx4 v[14:17], v[18:19], off offset:3072
	s_nop 0
	global_load_dwordx4 v[18:21], v[34:35], off
	global_load_dwordx4 v[22:25], v[34:35], off offset:1024
	global_load_dwordx4 v[26:29], v[34:35], off offset:2048
	global_load_dwordx4 v[30:33], v[34:35], off offset:3072
	v_or_b32_e32 v52, v147, v146
	s_add_i32 s0, s59, 2
	s_and_b32 s28, s0, 6
	s_or_b32 s31, s2, s28
	s_lshl_b32 s0, s31, 12
	v_lshl_add_u64 v[50:51], v[166:167], 0, s[0:1]
	s_waitcnt vmcnt(8) lgkmcnt(0)
	s_barrier
	global_load_dwordx4 v[34:37], v[50:51], off
	global_load_dwordx4 v[38:41], v[50:51], off offset:1024
	global_load_dwordx4 v[42:45], v[50:51], off offset:2048
	global_load_dwordx4 v[46:49], v[50:51], off offset:3072
	s_getreg_b32 s80, hwreg(HW_REG_XCC_ID, 0, 4)
	s_and_b32 s80, s80, 15
	s_add_i32 s80, s80, 1
	s_lshl_b32 s81, s34, 3
	s_or_b32 s81, s81, s33
	s_lshl_b32 s81, s81, 7
	s_add_u32 s82, s46, s81
	s_addc_u32 s83, s47, 0
	v_mov_b32_e32 v254, 0
	v_mov_b32_e32 v255, s80
	s_and_saveexec_b64 s[84:85], s[4:5]
	global_store_dword v254, v255, s[82:83] sc1
	s_mov_b64 exec, s[84:85]
	v_xad_u32 v191, v52, v152, 0
	v_lshl_add_u32 v122, s25, 10, v191
	ds_read_b128 v[50:53], v122
	ds_read_b128 v[54:57], v122 offset:16384
	ds_read_b128 v[58:61], v122 offset:32768
	ds_read_b128 v[62:65], v122 offset:49152
	s_setprio 1
	s_waitcnt vmcnt(11) lgkmcnt(3)
	v_mfma_f32_16x16x32_f16 v[66:69], v[2:5], v[50:53], 0
	s_waitcnt vmcnt(10)
	v_mfma_f32_16x16x32_f16 v[70:73], v[6:9], v[50:53], 0
	s_waitcnt vmcnt(9)
	v_mfma_f32_16x16x32_f16 v[74:77], v[10:13], v[50:53], 0
	s_waitcnt vmcnt(8)
	v_mfma_f32_16x16x32_f16 v[50:53], v[14:17], v[50:53], 0
	s_waitcnt lgkmcnt(2)
	v_mfma_f32_16x16x32_f16 v[78:81], v[2:5], v[54:57], 0
	v_mfma_f32_16x16x32_f16 v[82:85], v[6:9], v[54:57], 0
	v_mfma_f32_16x16x32_f16 v[86:89], v[10:13], v[54:57], 0
	v_mfma_f32_16x16x32_f16 v[54:57], v[14:17], v[54:57], 0
	s_waitcnt lgkmcnt(1)
	v_mfma_f32_16x16x32_f16 v[90:93], v[2:5], v[58:61], 0
	v_mfma_f32_16x16x32_f16 v[94:97], v[6:9], v[58:61], 0
	v_mfma_f32_16x16x32_f16 v[98:101], v[10:13], v[58:61], 0
	v_mfma_f32_16x16x32_f16 v[58:61], v[14:17], v[58:61], 0
	s_waitcnt lgkmcnt(0)
	v_mfma_f32_16x16x32_f16 v[102:105], v[2:5], v[62:65], 0
	v_mfma_f32_16x16x32_f16 v[106:109], v[6:9], v[62:65], 0
	v_mfma_f32_16x16x32_f16 v[110:113], v[10:13], v[62:65], 0
	v_mfma_f32_16x16x32_f16 v[62:65], v[14:17], v[62:65], 0
	s_setprio 0
	v_add_u32_e32 v114, 0x10000, v122
	v_add_u32_e32 v118, 0x14000, v122
	v_add_u32_e32 v123, 0x18000, v122
	v_add_u32_e32 v126, 0x1c000, v122
	ds_read_b128 v[114:117], v114
	ds_read_b128 v[118:121], v118
	ds_read_b128 v[122:125], v123
	ds_read_b128 v[126:129], v126
	s_setprio 1
	s_waitcnt lgkmcnt(3)
	v_mfma_f32_16x16x32_f16 v[130:133], v[2:5], v[114:117], 0
	v_mfma_f32_16x16x32_f16 v[134:137], v[6:9], v[114:117], 0
	v_mfma_f32_16x16x32_f16 v[138:141], v[10:13], v[114:117], 0
	v_mfma_f32_16x16x32_f16 v[114:117], v[14:17], v[114:117], 0
	s_waitcnt lgkmcnt(2)
	v_mfma_f32_16x16x32_f16 v[142:145], v[2:5], v[118:121], 0
	v_mfma_f32_16x16x32_f16 v[146:149], v[6:9], v[118:121], 0
	v_mfma_f32_16x16x32_f16 v[150:153], v[10:13], v[118:121], 0
	v_mfma_f32_16x16x32_f16 v[118:121], v[14:17], v[118:121], 0
	s_waitcnt lgkmcnt(1)
	v_mfma_f32_16x16x32_f16 v[154:157], v[2:5], v[122:125], 0
	v_mfma_f32_16x16x32_f16 v[158:161], v[6:9], v[122:125], 0
	v_mfma_f32_16x16x32_f16 v[170:173], v[10:13], v[122:125], 0
	v_mfma_f32_16x16x32_f16 v[122:125], v[14:17], v[122:125], 0
	s_waitcnt lgkmcnt(0)
	v_mfma_f32_16x16x32_f16 v[2:5], v[2:5], v[126:129], 0
	v_mfma_f32_16x16x32_f16 v[6:9], v[6:9], v[126:129], 0
	v_mfma_f32_16x16x32_f16 v[10:13], v[10:13], v[126:129], 0
	v_mfma_f32_16x16x32_f16 v[14:17], v[14:17], v[126:129], 0
	s_setprio 0
	s_add_i32 s0, s50, 3
	s_and_b32 s29, s0, 7
	s_or_b32 s48, s29, s2
	s_lshl_b32 s0, s48, 12
	v_lshl_add_u64 v[178:179], v[166:167], 0, s[0:1]
	global_load_dwordx4 v[126:129], v[178:179], off
	global_load_dwordx4 v[174:177], v[178:179], off offset:1024
	global_load_dwordx4 v[192:195], v[178:179], off offset:2048
	global_load_dwordx4 v[196:199], v[178:179], off offset:3072
	v_lshl_add_u32 v163, s30, 10, v191
	ds_read_b128 v[200:203], v163
	ds_read_b128 v[204:207], v163 offset:16384
	ds_read_b128 v[208:211], v163 offset:32768
	ds_read_b128 v[212:215], v163 offset:49152
	s_setprio 1
	s_waitcnt vmcnt(11) lgkmcnt(3)
	v_mfma_f32_16x16x32_f16 v[66:69], v[18:21], v[200:203], v[66:69]
	s_waitcnt vmcnt(10)
	v_mfma_f32_16x16x32_f16 v[70:73], v[22:25], v[200:203], v[70:73]
	s_waitcnt vmcnt(9)
	v_mfma_f32_16x16x32_f16 v[74:77], v[26:29], v[200:203], v[74:77]
	s_waitcnt vmcnt(8)
	v_mfma_f32_16x16x32_f16 v[50:53], v[30:33], v[200:203], v[50:53]
	s_waitcnt lgkmcnt(2)
	v_mfma_f32_16x16x32_f16 v[78:81], v[18:21], v[204:207], v[78:81]
	v_mfma_f32_16x16x32_f16 v[82:85], v[22:25], v[204:207], v[82:85]
	v_mfma_f32_16x16x32_f16 v[86:89], v[26:29], v[204:207], v[86:89]
	v_mfma_f32_16x16x32_f16 v[54:57], v[30:33], v[204:207], v[54:57]
	s_waitcnt lgkmcnt(1)
	v_mfma_f32_16x16x32_f16 v[90:93], v[18:21], v[208:211], v[90:93]
	v_mfma_f32_16x16x32_f16 v[94:97], v[22:25], v[208:211], v[94:97]
	v_mfma_f32_16x16x32_f16 v[98:101], v[26:29], v[208:211], v[98:101]
	v_mfma_f32_16x16x32_f16 v[58:61], v[30:33], v[208:211], v[58:61]
	s_waitcnt lgkmcnt(0)
	v_mfma_f32_16x16x32_f16 v[102:105], v[18:21], v[212:215], v[102:105]
	v_mfma_f32_16x16x32_f16 v[106:109], v[22:25], v[212:215], v[106:109]
	v_mfma_f32_16x16x32_f16 v[110:113], v[26:29], v[212:215], v[110:113]
	v_mfma_f32_16x16x32_f16 v[62:65], v[30:33], v[212:215], v[62:65]
	s_setprio 0
	v_add_u32_e32 v165, 0x10000, v163
	v_add_u32_e32 v168, 0x14000, v163
	ds_read_b128 v[200:203], v165
	ds_read_b128 v[204:207], v168
	v_add_u32_e32 v165, 0x18000, v163
	v_add_u32_e32 v163, 0x1c000, v163
	ds_read_b128 v[208:211], v165
	ds_read_b128 v[212:215], v163
	s_setprio 1
	s_waitcnt lgkmcnt(3)
	v_mfma_f32_16x16x32_f16 v[130:133], v[18:21], v[200:203], v[130:133]
	v_mfma_f32_16x16x32_f16 v[134:137], v[22:25], v[200:203], v[134:137]
	v_mfma_f32_16x16x32_f16 v[138:141], v[26:29], v[200:203], v[138:141]
	v_mfma_f32_16x16x32_f16 v[114:117], v[30:33], v[200:203], v[114:117]
	s_waitcnt lgkmcnt(2)
	v_mfma_f32_16x16x32_f16 v[142:145], v[18:21], v[204:207], v[142:145]
	v_mfma_f32_16x16x32_f16 v[146:149], v[22:25], v[204:207], v[146:149]
	v_mfma_f32_16x16x32_f16 v[150:153], v[26:29], v[204:207], v[150:153]
	v_mfma_f32_16x16x32_f16 v[118:121], v[30:33], v[204:207], v[118:121]
	s_waitcnt lgkmcnt(1)
	v_mfma_f32_16x16x32_f16 v[154:157], v[18:21], v[208:211], v[154:157]
	v_mfma_f32_16x16x32_f16 v[158:161], v[22:25], v[208:211], v[158:161]
	v_mfma_f32_16x16x32_f16 v[122:125], v[30:33], v[208:211], v[122:125]
	s_waitcnt lgkmcnt(0)
	v_mfma_f32_16x16x32_f16 v[2:5], v[18:21], v[212:215], v[2:5]
	v_mfma_f32_16x16x32_f16 v[6:9], v[22:25], v[212:215], v[6:9]
	v_mfma_f32_16x16x32_f16 v[10:13], v[26:29], v[212:215], v[10:13]
	v_mfma_f32_16x16x32_f16 v[14:17], v[30:33], v[212:215], v[14:17]
	v_mfma_f32_16x16x32_f16 v[170:173], v[26:29], v[208:211], v[170:173]
	s_setprio 0
	s_xor_b32 s25, s25, 4
	s_lshl_b32 s0, s25, 12
	v_lshl_add_u64 v[30:31], v[166:167], 0, s[0:1]
	global_load_dwordx4 v[18:21], v[30:31], off
	global_load_dwordx4 v[22:25], v[30:31], off offset:1024
	global_load_dwordx4 v[26:29], v[30:31], off offset:2048
	s_nop 0
	global_load_dwordx4 v[30:33], v[30:31], off offset:3072
	v_lshl_add_u32 v163, s31, 10, v191
	ds_read_b128 v[200:203], v163
	ds_read_b128 v[204:207], v163 offset:16384
	ds_read_b128 v[208:211], v163 offset:32768
	ds_read_b128 v[212:215], v163 offset:49152
	s_setprio 1
	s_waitcnt vmcnt(11) lgkmcnt(3)
	v_mfma_f32_16x16x32_f16 v[66:69], v[34:37], v[200:203], v[66:69]
	s_waitcnt vmcnt(10)
	v_mfma_f32_16x16x32_f16 v[70:73], v[38:41], v[200:203], v[70:73]
	s_waitcnt vmcnt(9)
	v_mfma_f32_16x16x32_f16 v[74:77], v[42:45], v[200:203], v[74:77]
	s_waitcnt vmcnt(8)
	v_mfma_f32_16x16x32_f16 v[50:53], v[46:49], v[200:203], v[50:53]
	s_waitcnt lgkmcnt(2)
	v_mfma_f32_16x16x32_f16 v[78:81], v[34:37], v[204:207], v[78:81]
	v_mfma_f32_16x16x32_f16 v[82:85], v[38:41], v[204:207], v[82:85]
	v_mfma_f32_16x16x32_f16 v[86:89], v[42:45], v[204:207], v[86:89]
	v_mfma_f32_16x16x32_f16 v[54:57], v[46:49], v[204:207], v[54:57]
	s_waitcnt lgkmcnt(1)
	v_mfma_f32_16x16x32_f16 v[90:93], v[34:37], v[208:211], v[90:93]
	v_mfma_f32_16x16x32_f16 v[94:97], v[38:41], v[208:211], v[94:97]
	v_mfma_f32_16x16x32_f16 v[98:101], v[42:45], v[208:211], v[98:101]
	v_mfma_f32_16x16x32_f16 v[58:61], v[46:49], v[208:211], v[58:61]
	s_waitcnt lgkmcnt(0)
	v_mfma_f32_16x16x32_f16 v[102:105], v[34:37], v[212:215], v[102:105]
	v_mfma_f32_16x16x32_f16 v[106:109], v[38:41], v[212:215], v[106:109]
	v_mfma_f32_16x16x32_f16 v[110:113], v[42:45], v[212:215], v[110:113]
	v_mfma_f32_16x16x32_f16 v[62:65], v[46:49], v[212:215], v[62:65]
	s_setprio 0
	v_add_u32_e32 v165, 0x10000, v163
	v_add_u32_e32 v168, 0x14000, v163
	ds_read_b128 v[200:203], v165
	ds_read_b128 v[204:207], v168
	v_add_u32_e32 v165, 0x18000, v163
	v_add_u32_e32 v163, 0x1c000, v163
	ds_read_b128 v[208:211], v165
	ds_read_b128 v[212:215], v163
	s_setprio 1
	s_waitcnt lgkmcnt(3)
	v_mfma_f32_16x16x32_f16 v[130:133], v[34:37], v[200:203], v[130:133]
	v_mfma_f32_16x16x32_f16 v[134:137], v[38:41], v[200:203], v[134:137]
	v_mfma_f32_16x16x32_f16 v[138:141], v[42:45], v[200:203], v[138:141]
	v_mfma_f32_16x16x32_f16 v[114:117], v[46:49], v[200:203], v[114:117]
	s_waitcnt lgkmcnt(2)
	v_mfma_f32_16x16x32_f16 v[142:145], v[34:37], v[204:207], v[142:145]
	v_mfma_f32_16x16x32_f16 v[146:149], v[38:41], v[204:207], v[146:149]
	v_mfma_f32_16x16x32_f16 v[150:153], v[42:45], v[204:207], v[150:153]
	v_mfma_f32_16x16x32_f16 v[118:121], v[46:49], v[204:207], v[118:121]
	s_waitcnt lgkmcnt(1)
	v_mfma_f32_16x16x32_f16 v[154:157], v[34:37], v[208:211], v[154:157]
	v_mfma_f32_16x16x32_f16 v[158:161], v[38:41], v[208:211], v[158:161]
	v_mfma_f32_16x16x32_f16 v[122:125], v[46:49], v[208:211], v[122:125]
	s_waitcnt lgkmcnt(0)
	v_mfma_f32_16x16x32_f16 v[2:5], v[34:37], v[212:215], v[2:5]
	v_mfma_f32_16x16x32_f16 v[6:9], v[38:41], v[212:215], v[6:9]
	v_mfma_f32_16x16x32_f16 v[10:13], v[42:45], v[212:215], v[10:13]
	v_mfma_f32_16x16x32_f16 v[14:17], v[46:49], v[212:215], v[14:17]
	v_mfma_f32_16x16x32_f16 v[170:173], v[42:45], v[208:211], v[170:173]
	s_setprio 0
	s_add_i32 s0, s50, 5
	s_and_b32 s30, s0, 7
	s_or_b32 s49, s30, s2
	s_lshl_b32 s0, s49, 12
	v_lshl_add_u64 v[46:47], v[166:167], 0, s[0:1]
	global_load_dwordx4 v[34:37], v[46:47], off
	global_load_dwordx4 v[38:41], v[46:47], off offset:1024
	global_load_dwordx4 v[42:45], v[46:47], off offset:2048
	s_nop 0
	global_load_dwordx4 v[46:49], v[46:47], off offset:3072
	v_lshl_add_u32 v163, s48, 10, v191
	ds_read_b128 v[200:203], v163
	ds_read_b128 v[204:207], v163 offset:16384
	ds_read_b128 v[208:211], v163 offset:32768
	ds_read_b128 v[212:215], v163 offset:49152
	s_setprio 1
	s_waitcnt vmcnt(11) lgkmcnt(3)
	v_mfma_f32_16x16x32_f16 v[66:69], v[126:129], v[200:203], v[66:69]
	s_waitcnt vmcnt(10)
	v_mfma_f32_16x16x32_f16 v[70:73], v[174:177], v[200:203], v[70:73]
	s_waitcnt vmcnt(9)
	v_mfma_f32_16x16x32_f16 v[74:77], v[192:195], v[200:203], v[74:77]
	s_waitcnt vmcnt(8)
	v_mfma_f32_16x16x32_f16 v[50:53], v[196:199], v[200:203], v[50:53]
	s_waitcnt lgkmcnt(2)
	v_mfma_f32_16x16x32_f16 v[78:81], v[126:129], v[204:207], v[78:81]
	v_mfma_f32_16x16x32_f16 v[82:85], v[174:177], v[204:207], v[82:85]
	v_mfma_f32_16x16x32_f16 v[86:89], v[192:195], v[204:207], v[86:89]
	v_mfma_f32_16x16x32_f16 v[54:57], v[196:199], v[204:207], v[54:57]
	s_waitcnt lgkmcnt(1)
	v_mfma_f32_16x16x32_f16 v[90:93], v[126:129], v[208:211], v[90:93]
	v_mfma_f32_16x16x32_f16 v[94:97], v[174:177], v[208:211], v[94:97]
	v_mfma_f32_16x16x32_f16 v[98:101], v[192:195], v[208:211], v[98:101]
	v_mfma_f32_16x16x32_f16 v[58:61], v[196:199], v[208:211], v[58:61]
	s_waitcnt lgkmcnt(0)
	v_mfma_f32_16x16x32_f16 v[102:105], v[126:129], v[212:215], v[102:105]
	v_mfma_f32_16x16x32_f16 v[106:109], v[174:177], v[212:215], v[106:109]
	v_mfma_f32_16x16x32_f16 v[110:113], v[192:195], v[212:215], v[110:113]
	v_mfma_f32_16x16x32_f16 v[62:65], v[196:199], v[212:215], v[62:65]
	s_setprio 0
	v_add_u32_e32 v165, 0x10000, v163
	v_add_u32_e32 v168, 0x14000, v163
	ds_read_b128 v[200:203], v165
	ds_read_b128 v[204:207], v168
	v_add_u32_e32 v165, 0x18000, v163
	v_add_u32_e32 v163, 0x1c000, v163
	ds_read_b128 v[208:211], v165
	ds_read_b128 v[212:215], v163
	s_setprio 1
	s_waitcnt lgkmcnt(3)
	v_mfma_f32_16x16x32_f16 v[130:133], v[126:129], v[200:203], v[130:133]
	v_mfma_f32_16x16x32_f16 v[134:137], v[174:177], v[200:203], v[134:137]
	v_mfma_f32_16x16x32_f16 v[138:141], v[192:195], v[200:203], v[138:141]
	v_mfma_f32_16x16x32_f16 v[114:117], v[196:199], v[200:203], v[114:117]
	s_waitcnt lgkmcnt(2)
	v_mfma_f32_16x16x32_f16 v[142:145], v[126:129], v[204:207], v[142:145]
	v_mfma_f32_16x16x32_f16 v[146:149], v[174:177], v[204:207], v[146:149]
	v_mfma_f32_16x16x32_f16 v[150:153], v[192:195], v[204:207], v[150:153]
	v_mfma_f32_16x16x32_f16 v[118:121], v[196:199], v[204:207], v[118:121]
	s_waitcnt lgkmcnt(1)
	v_mfma_f32_16x16x32_f16 v[154:157], v[126:129], v[208:211], v[154:157]
	v_mfma_f32_16x16x32_f16 v[158:161], v[174:177], v[208:211], v[158:161]
	v_mfma_f32_16x16x32_f16 v[122:125], v[196:199], v[208:211], v[122:125]
	s_waitcnt lgkmcnt(0)
	v_mfma_f32_16x16x32_f16 v[2:5], v[126:129], v[212:215], v[2:5]
	v_mfma_f32_16x16x32_f16 v[6:9], v[174:177], v[212:215], v[6:9]
	v_mfma_f32_16x16x32_f16 v[10:13], v[192:195], v[212:215], v[10:13]
	v_mfma_f32_16x16x32_f16 v[14:17], v[196:199], v[212:215], v[14:17]
	v_mfma_f32_16x16x32_f16 v[170:173], v[192:195], v[208:211], v[170:173]
	s_setprio 0
	s_add_i32 s59, s59, 6
	s_and_b32 s31, s59, 6
	s_or_b32 s52, s2, s31
	s_lshl_b32 s0, s52, 12
	v_lshl_add_u64 v[178:179], v[166:167], 0, s[0:1]
	s_lshl_b32 s86, s34, 3
	s_or_b32 s86, s86, s33
	s_xor_b32 s86, s86, 1
	s_lshl_b32 s86, s86, 7
	s_add_u32 s86, s46, s86
	s_addc_u32 s87, s47, 0
	v_mov_b32_e32 v254, 0
	global_load_dword v254, v254, s[86:87] sc1
	global_load_dwordx4 v[126:129], v[178:179], off
	global_load_dwordx4 v[174:177], v[178:179], off offset:1024
	global_load_dwordx4 v[192:195], v[178:179], off offset:2048
	global_load_dwordx4 v[196:199], v[178:179], off offset:3072
	v_lshl_add_u32 v163, s25, 10, v191
	ds_read_b128 v[200:203], v163
	ds_read_b128 v[204:207], v163 offset:16384
	ds_read_b128 v[208:211], v163 offset:32768
	ds_read_b128 v[212:215], v163 offset:49152
	s_setprio 1
	s_waitcnt vmcnt(12) lgkmcnt(3)
	v_mfma_f32_16x16x32_f16 v[66:69], v[18:21], v[200:203], v[66:69]
	s_waitcnt vmcnt(11)
	v_mfma_f32_16x16x32_f16 v[70:73], v[22:25], v[200:203], v[70:73]
	s_waitcnt vmcnt(10)
	v_mfma_f32_16x16x32_f16 v[74:77], v[26:29], v[200:203], v[74:77]
	s_waitcnt vmcnt(9)
	v_mfma_f32_16x16x32_f16 v[50:53], v[30:33], v[200:203], v[50:53]
	s_waitcnt lgkmcnt(2)
	v_mfma_f32_16x16x32_f16 v[78:81], v[18:21], v[204:207], v[78:81]
	v_mfma_f32_16x16x32_f16 v[82:85], v[22:25], v[204:207], v[82:85]
	v_mfma_f32_16x16x32_f16 v[86:89], v[26:29], v[204:207], v[86:89]
	v_mfma_f32_16x16x32_f16 v[54:57], v[30:33], v[204:207], v[54:57]
	s_waitcnt lgkmcnt(1)
	v_mfma_f32_16x16x32_f16 v[90:93], v[18:21], v[208:211], v[90:93]
	v_mfma_f32_16x16x32_f16 v[94:97], v[22:25], v[208:211], v[94:97]
	v_mfma_f32_16x16x32_f16 v[98:101], v[26:29], v[208:211], v[98:101]
	v_mfma_f32_16x16x32_f16 v[58:61], v[30:33], v[208:211], v[58:61]
	s_waitcnt lgkmcnt(0)
	v_mfma_f32_16x16x32_f16 v[102:105], v[18:21], v[212:215], v[102:105]
	v_mfma_f32_16x16x32_f16 v[106:109], v[22:25], v[212:215], v[106:109]
	v_mfma_f32_16x16x32_f16 v[110:113], v[26:29], v[212:215], v[110:113]
	v_mfma_f32_16x16x32_f16 v[62:65], v[30:33], v[212:215], v[62:65]
	s_setprio 0
	v_add_u32_e32 v165, 0x10000, v163
	v_add_u32_e32 v168, 0x14000, v163
	ds_read_b128 v[200:203], v165
	ds_read_b128 v[204:207], v168
	v_add_u32_e32 v165, 0x18000, v163
	v_add_u32_e32 v163, 0x1c000, v163
	ds_read_b128 v[208:211], v165
	ds_read_b128 v[212:215], v163
	s_setprio 1
	s_waitcnt lgkmcnt(3)
	v_mfma_f32_16x16x32_f16 v[130:133], v[18:21], v[200:203], v[130:133]
	v_mfma_f32_16x16x32_f16 v[134:137], v[22:25], v[200:203], v[134:137]
	v_mfma_f32_16x16x32_f16 v[138:141], v[26:29], v[200:203], v[138:141]
	v_mfma_f32_16x16x32_f16 v[114:117], v[30:33], v[200:203], v[114:117]
	s_waitcnt lgkmcnt(2)
	v_mfma_f32_16x16x32_f16 v[142:145], v[18:21], v[204:207], v[142:145]
	v_mfma_f32_16x16x32_f16 v[146:149], v[22:25], v[204:207], v[146:149]
	v_mfma_f32_16x16x32_f16 v[150:153], v[26:29], v[204:207], v[150:153]
	v_mfma_f32_16x16x32_f16 v[118:121], v[30:33], v[204:207], v[118:121]
	s_waitcnt lgkmcnt(1)
	v_mfma_f32_16x16x32_f16 v[154:157], v[18:21], v[208:211], v[154:157]
	v_mfma_f32_16x16x32_f16 v[158:161], v[22:25], v[208:211], v[158:161]
	v_mfma_f32_16x16x32_f16 v[122:125], v[30:33], v[208:211], v[122:125]
	s_waitcnt lgkmcnt(0)
	v_mfma_f32_16x16x32_f16 v[2:5], v[18:21], v[212:215], v[2:5]
	v_mfma_f32_16x16x32_f16 v[6:9], v[22:25], v[212:215], v[6:9]
	v_mfma_f32_16x16x32_f16 v[10:13], v[26:29], v[212:215], v[10:13]
	v_mfma_f32_16x16x32_f16 v[14:17], v[30:33], v[212:215], v[14:17]
	v_mfma_f32_16x16x32_f16 v[170:173], v[26:29], v[208:211], v[170:173]
	s_setprio 0
	s_add_i32 s0, s50, -1
	s_and_b32 s48, s0, 7
	s_or_b32 s25, s48, s2
	s_lshl_b32 s0, s25, 12
	v_lshl_add_u64 v[18:19], v[166:167], 0, s[0:1]
	global_load_dwordx4 v[200:203], v[18:19], off
	global_load_dwordx4 v[204:207], v[18:19], off offset:1024
	global_load_dwordx4 v[208:211], v[18:19], off offset:2048
	global_load_dwordx4 v[212:215], v[18:19], off offset:3072
	v_lshl_add_u32 v163, s49, 10, v191
	ds_read_b128 v[18:21], v163
	ds_read_b128 v[22:25], v163 offset:16384
	ds_read_b128 v[26:29], v163 offset:32768
	ds_read_b128 v[30:33], v163 offset:49152
	s_setprio 1
	s_waitcnt vmcnt(12) lgkmcnt(3)
	v_mfma_f32_16x16x32_f16 v[66:69], v[34:37], v[18:21], v[66:69]
	s_waitcnt vmcnt(11)
	v_mfma_f32_16x16x32_f16 v[70:73], v[38:41], v[18:21], v[70:73]
	s_waitcnt vmcnt(10)
	v_mfma_f32_16x16x32_f16 v[74:77], v[42:45], v[18:21], v[74:77]
	s_waitcnt vmcnt(9)
	v_mfma_f32_16x16x32_f16 v[18:21], v[46:49], v[18:21], v[50:53]
	s_waitcnt lgkmcnt(2)
	v_mfma_f32_16x16x32_f16 v[50:53], v[34:37], v[22:25], v[78:81]
	v_mfma_f32_16x16x32_f16 v[78:81], v[38:41], v[22:25], v[82:85]
	v_mfma_f32_16x16x32_f16 v[82:85], v[42:45], v[22:25], v[86:89]
	v_mfma_f32_16x16x32_f16 v[22:25], v[46:49], v[22:25], v[54:57]
	s_waitcnt lgkmcnt(1)
	v_mfma_f32_16x16x32_f16 v[54:57], v[34:37], v[26:29], v[90:93]
	v_mfma_f32_16x16x32_f16 v[86:89], v[38:41], v[26:29], v[94:97]
	v_mfma_f32_16x16x32_f16 v[90:93], v[42:45], v[26:29], v[98:101]
	v_mfma_f32_16x16x32_f16 v[26:29], v[46:49], v[26:29], v[58:61]
	s_waitcnt lgkmcnt(0)
	v_mfma_f32_16x16x32_f16 v[58:61], v[34:37], v[30:33], v[102:105]
	v_mfma_f32_16x16x32_f16 v[94:97], v[38:41], v[30:33], v[106:109]
	v_mfma_f32_16x16x32_f16 v[98:101], v[42:45], v[30:33], v[110:113]
	v_mfma_f32_16x16x32_f16 v[30:33], v[46:49], v[30:33], v[62:65]
	s_setprio 0
	s_nop 1
	v_add_u32_e32 v62, 0x10000, v163
	v_add_u32_e32 v102, 0x14000, v163
	v_add_u32_e32 v106, 0x18000, v163
	v_add_u32_e32 v110, 0x1c000, v163
	ds_read_b128 v[62:65], v62
	ds_read_b128 v[102:105], v102
	ds_read_b128 v[106:109], v106
	ds_read_b128 v[110:113], v110
	s_setprio 1
	s_waitcnt lgkmcnt(3)
	v_mfma_f32_16x16x32_f16 v[130:133], v[34:37], v[62:65], v[130:133]
	v_mfma_f32_16x16x32_f16 v[134:137], v[38:41], v[62:65], v[134:137]
	v_mfma_f32_16x16x32_f16 v[138:141], v[42:45], v[62:65], v[138:141]
	v_mfma_f32_16x16x32_f16 v[62:65], v[46:49], v[62:65], v[114:117]
	s_waitcnt lgkmcnt(2)
	v_mfma_f32_16x16x32_f16 v[114:117], v[34:37], v[102:105], v[142:145]
	v_mfma_f32_16x16x32_f16 v[142:145], v[38:41], v[102:105], v[146:149]
	v_mfma_f32_16x16x32_f16 v[146:149], v[42:45], v[102:105], v[150:153]
	v_mfma_f32_16x16x32_f16 v[102:105], v[46:49], v[102:105], v[118:121]
	s_waitcnt lgkmcnt(1)
	v_mfma_f32_16x16x32_f16 v[118:121], v[34:37], v[106:109], v[154:157]
	v_mfma_f32_16x16x32_f16 v[150:153], v[38:41], v[106:109], v[158:161]
	v_mfma_f32_16x16x32_f16 v[154:157], v[42:45], v[106:109], v[170:173]
	v_mfma_f32_16x16x32_f16 v[106:109], v[46:49], v[106:109], v[122:125]
	s_waitcnt lgkmcnt(0)
	v_mfma_f32_16x16x32_f16 v[34:37], v[34:37], v[110:113], v[2:5]
	v_mfma_f32_16x16x32_f16 v[38:41], v[38:41], v[110:113], v[6:9]
	v_mfma_f32_16x16x32_f16 v[42:45], v[42:45], v[110:113], v[10:13]
	v_mfma_f32_16x16x32_f16 v[46:49], v[46:49], v[110:113], v[14:17]
	s_setprio 0
	s_xor_b32 s2, s58, 1
	s_lshl_b32 s49, s2, 3
	s_or_b32 s51, s49, s50
	s_lshl_b32 s0, s51, 12
	v_lshl_add_u64 v[14:15], v[166:167], 0, s[0:1]
	s_waitcnt vmcnt(8)
	s_barrier
	v_lshlrev_b32_e32 v255, 4, v0
	v_readfirstlane_b32 s92, v0
	s_lshl_b32 s92, s92, 4
	s_xor_b32 s93, s58, 1
	s_lshl_b32 s94, s93, 13
	s_add_i32 s92, s92, s94
	s_lshl_b32 s94, s34, 3
	s_or_b32 s94, s94, s33
	s_xor_b32 s94, s94, 1
	s_lshl_b32 s94, s94, 16
	s_add_u32 s88, s26, s94
	s_addc_u32 s89, s27, 0
	s_add_i32 s95, s92, 0x0
	s_mov_b32 m0, s95
	s_add_u32 s84, s88, 0x0
	s_addc_u32 s85, s89, 0
	global_load_lds_dwordx4 v255, s[84:85] sc0 sc1
	s_add_i32 s95, s92, 0x4000
	s_mov_b32 m0, s95
	s_add_u32 s84, s88, 0x2000
	s_addc_u32 s85, s89, 0
	global_load_lds_dwordx4 v255, s[84:85] sc0 sc1
	s_add_i32 s95, s92, 0x8000
	s_mov_b32 m0, s95
	s_add_u32 s84, s88, 0x4000
	s_addc_u32 s85, s89, 0
	global_load_lds_dwordx4 v255, s[84:85] sc0 sc1
	s_add_i32 s95, s92, 0xc000
	s_mov_b32 m0, s95
	s_add_u32 s84, s88, 0x6000
	s_addc_u32 s85, s89, 0
	global_load_lds_dwordx4 v255, s[84:85] sc0 sc1
	s_add_i32 s95, s92, 0x10000
	s_mov_b32 m0, s95
	s_add_u32 s84, s88, 0x8000
	s_addc_u32 s85, s89, 0
	global_load_lds_dwordx4 v255, s[84:85] sc0 sc1
	s_add_i32 s95, s92, 0x14000
	s_mov_b32 m0, s95
	s_add_u32 s84, s88, 0xa000
	s_addc_u32 s85, s89, 0
	global_load_lds_dwordx4 v255, s[84:85] sc0 sc1
	s_add_i32 s95, s92, 0x18000
	s_mov_b32 m0, s95
	s_add_u32 s84, s88, 0xc000
	s_addc_u32 s85, s89, 0
	global_load_lds_dwordx4 v255, s[84:85] sc0 sc1
	s_add_i32 s95, s92, 0x1c000
	s_mov_b32 m0, s95
	s_add_u32 s84, s88, 0xe000
	s_addc_u32 s85, s89, 0
	global_load_lds_dwordx4 v255, s[84:85] sc0 sc1
	global_load_dwordx4 v[2:5], v[14:15], off
	global_load_dwordx4 v[6:9], v[14:15], off offset:1024
	global_load_dwordx4 v[10:13], v[14:15], off offset:2048
	s_nop 0
	global_load_dwordx4 v[14:17], v[14:15], off offset:3072
	v_lshl_add_u32 v163, s52, 10, v191
	ds_read_b128 v[110:113], v163
	ds_read_b128 v[122:125], v163 offset:16384
	ds_read_b128 v[158:161], v163 offset:32768
	ds_read_b128 v[170:173], v163 offset:49152
	s_setprio 1
	s_waitcnt vmcnt(19) lgkmcnt(3)
	v_mfma_f32_16x16x32_f16 v[66:69], v[126:129], v[110:113], v[66:69]
	s_waitcnt vmcnt(18)
	v_mfma_f32_16x16x32_f16 v[70:73], v[174:177], v[110:113], v[70:73]
	s_waitcnt vmcnt(17)
	v_mfma_f32_16x16x32_f16 v[74:77], v[192:195], v[110:113], v[74:77]
	s_waitcnt vmcnt(16)
	v_mfma_f32_16x16x32_f16 v[110:113], v[196:199], v[110:113], v[18:21]
	s_waitcnt lgkmcnt(2)
	v_mfma_f32_16x16x32_f16 v[50:53], v[126:129], v[122:125], v[50:53]
	v_mfma_f32_16x16x32_f16 v[78:81], v[174:177], v[122:125], v[78:81]
	v_mfma_f32_16x16x32_f16 v[82:85], v[192:195], v[122:125], v[82:85]
	v_mfma_f32_16x16x32_f16 v[122:125], v[196:199], v[122:125], v[22:25]
	s_waitcnt lgkmcnt(1)
	v_mfma_f32_16x16x32_f16 v[216:219], v[126:129], v[158:161], v[54:57]
	v_mfma_f32_16x16x32_f16 v[86:89], v[174:177], v[158:161], v[86:89]
	v_mfma_f32_16x16x32_f16 v[90:93], v[192:195], v[158:161], v[90:93]
	v_mfma_f32_16x16x32_f16 v[158:161], v[196:199], v[158:161], v[26:29]
	s_waitcnt lgkmcnt(0)
	v_mfma_f32_16x16x32_f16 v[94:97], v[174:177], v[170:173], v[94:97]
	v_mfma_f32_16x16x32_f16 v[98:101], v[192:195], v[170:173], v[98:101]
	v_mfma_f32_16x16x32_f16 v[220:223], v[126:129], v[170:173], v[58:61]
	v_mfma_f32_16x16x32_f16 v[170:173], v[196:199], v[170:173], v[30:33]
	s_setprio 0
	v_add_u32_e32 v18, 0x10000, v163
	v_add_u32_e32 v22, 0x14000, v163
	v_add_u32_e32 v26, 0x18000, v163
	v_add_u32_e32 v30, 0x1c000, v163
	ds_read_b128 v[18:21], v18
	ds_read_b128 v[22:25], v22
	ds_read_b128 v[26:29], v26
	ds_read_b128 v[30:33], v30
	s_setprio 1
	s_waitcnt lgkmcnt(3)
	v_mfma_f32_16x16x32_f16 v[130:133], v[126:129], v[18:21], v[130:133]
	v_mfma_f32_16x16x32_f16 v[134:137], v[174:177], v[18:21], v[134:137]
	v_mfma_f32_16x16x32_f16 v[138:141], v[192:195], v[18:21], v[138:141]
	s_waitcnt lgkmcnt(2)
	v_mfma_f32_16x16x32_f16 v[114:117], v[126:129], v[22:25], v[114:117]
	v_mfma_f32_16x16x32_f16 v[142:145], v[174:177], v[22:25], v[142:145]
	v_mfma_f32_16x16x32_f16 v[146:149], v[192:195], v[22:25], v[146:149]
	s_waitcnt lgkmcnt(1)
	v_mfma_f32_16x16x32_f16 v[150:153], v[174:177], v[26:29], v[150:153]
	v_mfma_f32_16x16x32_f16 v[154:157], v[192:195], v[26:29], v[154:157]
	v_mfma_f32_16x16x32_f16 v[224:227], v[196:199], v[18:21], v[62:65]
	v_mfma_f32_16x16x32_f16 v[228:231], v[196:199], v[22:25], v[102:105]
	v_mfma_f32_16x16x32_f16 v[232:235], v[126:129], v[26:29], v[118:121]
	v_mfma_f32_16x16x32_f16 v[236:239], v[196:199], v[26:29], v[106:109]
	s_waitcnt lgkmcnt(0)
	v_mfma_f32_16x16x32_f16 v[240:243], v[126:129], v[30:33], v[34:37]
	v_mfma_f32_16x16x32_f16 v[174:177], v[174:177], v[30:33], v[38:41]
	v_mfma_f32_16x16x32_f16 v[192:195], v[192:195], v[30:33], v[42:45]
	v_mfma_f32_16x16x32_f16 v[196:199], v[196:199], v[30:33], v[46:49]
	s_setprio 0
	s_or_b32 s52, s49, s24
	s_lshl_b32 s0, s52, 12
	v_lshl_add_u64 v[30:31], v[166:167], 0, s[0:1]
	global_load_dwordx4 v[18:21], v[30:31], off
	global_load_dwordx4 v[22:25], v[30:31], off offset:1024
	global_load_dwordx4 v[26:29], v[30:31], off offset:2048
	s_nop 0
	global_load_dwordx4 v[30:33], v[30:31], off offset:3072
	v_lshl_add_u32 v118, s25, 10, v191
	ds_read_b128 v[46:49], v118
	ds_read_b128 v[62:65], v118 offset:16384
	ds_read_b128 v[102:105], v118 offset:32768
	ds_read_b128 v[106:109], v118 offset:49152
	s_setprio 1
	s_waitcnt vmcnt(19) lgkmcnt(3)
	v_mfma_f32_16x16x32_f16 v[34:37], v[200:203], v[46:49], v[66:69]
	s_waitcnt vmcnt(18)
	v_mfma_f32_16x16x32_f16 v[38:41], v[204:207], v[46:49], v[70:73]
	s_waitcnt vmcnt(17)
	v_mfma_f32_16x16x32_f16 v[42:45], v[208:211], v[46:49], v[74:77]
	s_waitcnt vmcnt(16)
	v_mfma_f32_16x16x32_f16 v[46:49], v[212:215], v[46:49], v[110:113]
	s_waitcnt lgkmcnt(2)
	v_mfma_f32_16x16x32_f16 v[50:53], v[200:203], v[62:65], v[50:53]
	v_mfma_f32_16x16x32_f16 v[54:57], v[204:207], v[62:65], v[78:81]
	v_mfma_f32_16x16x32_f16 v[58:61], v[208:211], v[62:65], v[82:85]
	v_mfma_f32_16x16x32_f16 v[62:65], v[212:215], v[62:65], v[122:125]
	s_waitcnt lgkmcnt(1)
	v_mfma_f32_16x16x32_f16 v[66:69], v[200:203], v[102:105], v[216:219]
	v_mfma_f32_16x16x32_f16 v[70:73], v[204:207], v[102:105], v[86:89]
	v_mfma_f32_16x16x32_f16 v[74:77], v[208:211], v[102:105], v[90:93]
	v_mfma_f32_16x16x32_f16 v[78:81], v[212:215], v[102:105], v[158:161]
	s_waitcnt lgkmcnt(0)
	v_mfma_f32_16x16x32_f16 v[82:85], v[200:203], v[106:109], v[220:223]
	v_mfma_f32_16x16x32_f16 v[86:89], v[204:207], v[106:109], v[94:97]
	v_mfma_f32_16x16x32_f16 v[90:93], v[208:211], v[106:109], v[98:101]
	v_mfma_f32_16x16x32_f16 v[94:97], v[212:215], v[106:109], v[170:173]
	s_setprio 0
	s_nop 0
	v_add_u32_e32 v98, 0x10000, v118
	v_add_u32_e32 v99, 0x14000, v118
	ds_read_b128 v[110:113], v98
	ds_read_b128 v[126:129], v99
	v_add_u32_e32 v98, 0x18000, v118
	v_add_u32_e32 v99, 0x1c000, v118
	ds_read_b128 v[158:161], v98
	ds_read_b128 v[170:173], v99
	s_setprio 1
	s_waitcnt lgkmcnt(3)
	v_mfma_f32_16x16x32_f16 v[98:101], v[200:203], v[110:113], v[130:133]
	v_mfma_f32_16x16x32_f16 v[102:105], v[204:207], v[110:113], v[134:137]
	v_mfma_f32_16x16x32_f16 v[106:109], v[208:211], v[110:113], v[138:141]
	v_mfma_f32_16x16x32_f16 v[110:113], v[212:215], v[110:113], v[224:227]
	s_waitcnt lgkmcnt(2)
	v_mfma_f32_16x16x32_f16 v[114:117], v[200:203], v[126:129], v[114:117]
	v_mfma_f32_16x16x32_f16 v[118:121], v[204:207], v[126:129], v[142:145]
	v_mfma_f32_16x16x32_f16 v[122:125], v[208:211], v[126:129], v[146:149]
	v_mfma_f32_16x16x32_f16 v[126:129], v[212:215], v[126:129], v[228:231]
	s_waitcnt lgkmcnt(1)
	v_mfma_f32_16x16x32_f16 v[130:133], v[200:203], v[158:161], v[232:235]
	v_mfma_f32_16x16x32_f16 v[134:137], v[204:207], v[158:161], v[150:153]
	v_mfma_f32_16x16x32_f16 v[138:141], v[208:211], v[158:161], v[154:157]
	v_mfma_f32_16x16x32_f16 v[142:145], v[212:215], v[158:161], v[236:239]
	s_waitcnt lgkmcnt(0)
	v_mfma_f32_16x16x32_f16 v[146:149], v[200:203], v[170:173], v[240:243]
	v_mfma_f32_16x16x32_f16 v[150:153], v[204:207], v[170:173], v[174:177]
	v_mfma_f32_16x16x32_f16 v[154:157], v[208:211], v[170:173], v[192:195]
	v_mfma_f32_16x16x32_f16 v[158:161], v[212:215], v[170:173], v[196:199]
	s_setprio 0
	s_waitcnt vmcnt(0)
	s_barrier
	s_getreg_b32 s24, hwreg(HW_REG_XCC_ID, 0, 4)
	s_and_saveexec_b64 s[0:1], s[4:5]
	s_cbranch_execz .LBB5_145
	s_and_b32 s53, s24, 15
	s_lshl_b32 s24, s34, 3
	s_or_b32 s50, s24, s50
	s_or_b32 s24, s50, s58
	s_lshl_b32 s24, s24, 5
	s_ashr_i32 s25, s24, 31
	s_lshl_b64 s[24:25], s[24:25], 2
	s_add_u32 s24, s46, s24
	s_addc_u32 s25, s47, s25
	s_add_i32 s54, s53, 1
	v_mov_b32_e32 v163, s54
	s_or_b32 s24, s50, s2
	s_lshl_b32 s24, s24, 5
	s_ashr_i32 s25, s24, 31
	s_lshl_b64 s[24:25], s[24:25], 2
	s_add_u32 s24, s46, s24
	s_addc_u32 s25, s47, s25
	s_mov_b32 s90, 0
	v_mov_b32_e32 v163, v254
	v_cmp_ne_u32_e32 vcc, 0, v163
	s_cbranch_vccnz .LBB5_144
	s_mov_b32 s90, 2
	v_mov_b32_e32 v165, 0

.LBB5_144:
	v_add_u32_e32 v163, -1, v163
	v_cmp_eq_u32_e32 vcc, s53, v163
	s_add_i32 s24, 0, 0x20000
	v_mov_b32_e32 v165, s24
	v_cndmask_b32_e64 v163, 0, 1, vcc
	v_or_b32_e32 v163, s90, v163
	ds_write_b32 v165, v163
.LBB5_145:
	s_or_b64 exec, exec, s[0:1]
	s_add_i32 s24, 0, 0x20000
	v_mov_b32_e32 v163, s24
	s_waitcnt lgkmcnt(0)
	s_barrier
	ds_read_b32 v163, v163
	s_or_b32 s2, s7, s2
	s_lshl_b64 s[0:1], s[2:3], 16
	s_add_u32 s0, s26, s0
	s_addc_u32 s1, s27, s1
	s_waitcnt lgkmcnt(0)
	v_readfirstlane_b32 s91, v163
	s_bitcmp1_b32 s91, 1
	s_cbranch_scc0 .Lex_skip
	v_and_b32_e32 v163, 1, v163
	v_cmp_eq_u32_e32 vcc, 0, v163
	v_and_b32_e32 v163, 0x3f0, v162
	v_add_u32_e32 v192, 0, v163
	v_mov_b32_e32 v163, 0
	v_mov_b32_e32 v165, v163
	v_or_b32_e32 v172, s49, v187
	v_lshl_add_u64 v[170:171], s[0:1], 0, v[164:165]
	v_lshrrev_b32_e32 v164, 9, v164
	v_lshlrev_b32_e32 v193, 10, v172
	v_and_or_b32 v164, v164, 16, v172
	v_lshl_add_u64 v[168:169], s[0:1], 0, v[162:163]
	v_lshlrev_b32_e32 v194, 10, v164
	v_or_b32_e32 v164, 0x4000, v162
	v_or_b32_e32 v195, 0x8000, v193
	v_or_b32_e32 v172, 0x6000, v162
	v_mov_b32_e32 v173, v163
	v_or_b32_e32 v196, 0xc000, v193
	v_or_b32_e32 v174, 0x8000, v162
	v_mov_b32_e32 v175, v163
	v_or_b32_e32 v200, 0x10000, v193
	v_or_b32_e32 v176, 0xa000, v162
	v_mov_b32_e32 v177, v163
	v_or_b32_e32 v201, 0x14000, v193
	v_or_b32_e32 v178, 0xc000, v162
	v_mov_b32_e32 v179, v163
	v_or_b32_e32 v202, 0x18000, v193
	v_or_b32_e32 v162, 0xe000, v162
	v_or_b32_e32 v203, 0x1c000, v193
	v_lshl_add_u64 v[164:165], s[0:1], 0, v[164:165]
	v_lshl_add_u64 v[172:173], s[0:1], 0, v[172:173]
	v_lshl_add_u64 v[174:175], s[0:1], 0, v[174:175]
	v_lshl_add_u64 v[176:177], s[0:1], 0, v[176:177]
	v_lshl_add_u64 v[178:179], s[0:1], 0, v[178:179]
	v_lshl_add_u64 v[162:163], s[0:1], 0, v[162:163]
	s_and_b64 vcc, exec, vcc
	v_add_u32_e32 v199, v192, v193
	v_add_u32_e32 v198, v192, v194
	v_add_u32_e32 v197, v192, v195
	v_add_u32_e32 v196, v192, v196
	v_add_u32_e32 v195, v192, v200
	v_add_u32_e32 v194, v192, v201
	v_add_u32_e32 v193, v192, v202
	v_add_u32_e32 v192, v192, v203
	s_cbranch_vccnz .LBB5_185
	v_readfirstlane_b32 s0, v199
	s_mov_b32 m0, s0
	v_readfirstlane_b32 s0, v198
	global_load_lds_dwordx4 v[168:169], off
	s_mov_b32 m0, s0
	v_readfirstlane_b32 s0, v197
	global_load_lds_dwordx4 v[170:171], off
	s_mov_b32 m0, s0
	v_readfirstlane_b32 s0, v196
	global_load_lds_dwordx4 v[164:165], off
	s_mov_b32 m0, s0
	v_readfirstlane_b32 s0, v195
	global_load_lds_dwordx4 v[172:173], off
	s_mov_b32 m0, s0
	v_readfirstlane_b32 s0, v194
	global_load_lds_dwordx4 v[174:175], off
	s_mov_b32 m0, s0
	v_readfirstlane_b32 s0, v193
	global_load_lds_dwordx4 v[176:177], off
	s_mov_b32 m0, s0
	v_readfirstlane_b32 s0, v192
	global_load_lds_dwordx4 v[178:179], off
	s_mov_b32 m0, s0
	s_nop 0
	global_load_lds_dwordx4 v[162:163], off
	s_cbranch_execnz .LBB5_148

.Lex_skip:
.LBB5_148:
	s_or_b32 s2, s49, s28
	s_lshl_b32 s0, s2, 12
	s_mov_b32 s1, 0
	v_lshl_add_u64 v[176:177], v[166:167], 0, s[0:1]
	s_waitcnt vmcnt(0)
	s_waitcnt vmcnt(0) lgkmcnt(0)
	s_barrier
	global_load_dwordx4 v[162:165], v[176:177], off
	global_load_dwordx4 v[168:171], v[176:177], off offset:1024
	global_load_dwordx4 v[172:175], v[176:177], off offset:2048
	s_nop 0
	global_load_dwordx4 v[176:179], v[176:177], off offset:3072
	v_lshl_add_u32 v208, s51, 10, v191
	ds_read_b128 v[192:195], v208
	ds_read_b128 v[196:199], v208 offset:16384
	ds_read_b128 v[200:203], v208 offset:32768
	ds_read_b128 v[204:207], v208 offset:49152
	s_setprio 1
	s_waitcnt lgkmcnt(3)
	v_mfma_f32_16x16x32_f16 v[34:37], v[2:5], v[192:195], v[34:37]
	v_mfma_f32_16x16x32_f16 v[38:41], v[6:9], v[192:195], v[38:41]
	v_mfma_f32_16x16x32_f16 v[42:45], v[10:13], v[192:195], v[42:45]
	v_mfma_f32_16x16x32_f16 v[46:49], v[14:17], v[192:195], v[46:49]
	s_waitcnt lgkmcnt(2)
	v_mfma_f32_16x16x32_f16 v[50:53], v[2:5], v[196:199], v[50:53]
	v_mfma_f32_16x16x32_f16 v[54:57], v[6:9], v[196:199], v[54:57]
	v_mfma_f32_16x16x32_f16 v[58:61], v[10:13], v[196:199], v[58:61]
	v_mfma_f32_16x16x32_f16 v[62:65], v[14:17], v[196:199], v[62:65]
	s_waitcnt lgkmcnt(1)
	v_mfma_f32_16x16x32_f16 v[66:69], v[2:5], v[200:203], v[66:69]
	v_mfma_f32_16x16x32_f16 v[70:73], v[6:9], v[200:203], v[70:73]
	v_mfma_f32_16x16x32_f16 v[74:77], v[10:13], v[200:203], v[74:77]
	v_mfma_f32_16x16x32_f16 v[78:81], v[14:17], v[200:203], v[78:81]
	s_waitcnt lgkmcnt(0)
	v_mfma_f32_16x16x32_f16 v[82:85], v[2:5], v[204:207], v[82:85]
	v_mfma_f32_16x16x32_f16 v[86:89], v[6:9], v[204:207], v[86:89]
	v_mfma_f32_16x16x32_f16 v[90:93], v[10:13], v[204:207], v[90:93]
	v_mfma_f32_16x16x32_f16 v[94:97], v[14:17], v[204:207], v[94:97]
	s_setprio 0
	v_add_u32_e32 v192, 0x10000, v208
	v_add_u32_e32 v196, 0x14000, v208
	v_add_u32_e32 v200, 0x18000, v208
	v_add_u32_e32 v204, 0x1c000, v208
	ds_read_b128 v[192:195], v192
	ds_read_b128 v[196:199], v196
	ds_read_b128 v[200:203], v200
	ds_read_b128 v[204:207], v204
	s_setprio 1
	s_waitcnt lgkmcnt(3)
	v_mfma_f32_16x16x32_f16 v[98:101], v[2:5], v[192:195], v[98:101]
	v_mfma_f32_16x16x32_f16 v[102:105], v[6:9], v[192:195], v[102:105]
	v_mfma_f32_16x16x32_f16 v[106:109], v[10:13], v[192:195], v[106:109]
	v_mfma_f32_16x16x32_f16 v[110:113], v[14:17], v[192:195], v[110:113]
	s_waitcnt lgkmcnt(2)
	v_mfma_f32_16x16x32_f16 v[114:117], v[2:5], v[196:199], v[114:117]
	v_mfma_f32_16x16x32_f16 v[118:121], v[6:9], v[196:199], v[118:121]
	v_mfma_f32_16x16x32_f16 v[122:125], v[10:13], v[196:199], v[122:125]
	v_mfma_f32_16x16x32_f16 v[126:129], v[14:17], v[196:199], v[126:129]
	s_waitcnt lgkmcnt(1)
	v_mfma_f32_16x16x32_f16 v[130:133], v[2:5], v[200:203], v[130:133]
	v_mfma_f32_16x16x32_f16 v[134:137], v[6:9], v[200:203], v[134:137]
	v_mfma_f32_16x16x32_f16 v[138:141], v[10:13], v[200:203], v[138:141]
	v_mfma_f32_16x16x32_f16 v[142:145], v[14:17], v[200:203], v[142:145]
	s_waitcnt lgkmcnt(0)
	v_mfma_f32_16x16x32_f16 v[2:5], v[2:5], v[204:207], v[146:149]
	v_mfma_f32_16x16x32_f16 v[6:9], v[6:9], v[204:207], v[150:153]
	v_mfma_f32_16x16x32_f16 v[10:13], v[10:13], v[204:207], v[154:157]
	v_mfma_f32_16x16x32_f16 v[14:17], v[14:17], v[204:207], v[158:161]
	s_setprio 0
	s_or_b32 s3, s49, s29
	s_lshl_b32 s0, s3, 12
	v_lshl_add_u64 v[158:159], v[166:167], 0, s[0:1]
	global_load_dwordx4 v[146:149], v[158:159], off
	global_load_dwordx4 v[150:153], v[158:159], off offset:1024
	global_load_dwordx4 v[154:157], v[158:159], off offset:2048
	s_nop 0
	global_load_dwordx4 v[158:161], v[158:159], off offset:3072
	v_lshl_add_u32 v208, s52, 10, v191
	ds_read_b128 v[192:195], v208
	ds_read_b128 v[196:199], v208 offset:16384
	ds_read_b128 v[200:203], v208 offset:32768
	ds_read_b128 v[204:207], v208 offset:49152
	s_setprio 1
	s_waitcnt lgkmcnt(3)
	v_mfma_f32_16x16x32_f16 v[34:37], v[18:21], v[192:195], v[34:37]
	v_mfma_f32_16x16x32_f16 v[38:41], v[22:25], v[192:195], v[38:41]
	v_mfma_f32_16x16x32_f16 v[42:45], v[26:29], v[192:195], v[42:45]
	v_mfma_f32_16x16x32_f16 v[46:49], v[30:33], v[192:195], v[46:49]
	s_waitcnt lgkmcnt(2)
	v_mfma_f32_16x16x32_f16 v[50:53], v[18:21], v[196:199], v[50:53]
	v_mfma_f32_16x16x32_f16 v[54:57], v[22:25], v[196:199], v[54:57]
	v_mfma_f32_16x16x32_f16 v[58:61], v[26:29], v[196:199], v[58:61]
	v_mfma_f32_16x16x32_f16 v[62:65], v[30:33], v[196:199], v[62:65]
	s_waitcnt lgkmcnt(1)
	v_mfma_f32_16x16x32_f16 v[66:69], v[18:21], v[200:203], v[66:69]
	v_mfma_f32_16x16x32_f16 v[70:73], v[22:25], v[200:203], v[70:73]
	v_mfma_f32_16x16x32_f16 v[74:77], v[26:29], v[200:203], v[74:77]
	v_mfma_f32_16x16x32_f16 v[78:81], v[30:33], v[200:203], v[78:81]
	s_waitcnt lgkmcnt(0)
	v_mfma_f32_16x16x32_f16 v[82:85], v[18:21], v[204:207], v[82:85]
	v_mfma_f32_16x16x32_f16 v[86:89], v[22:25], v[204:207], v[86:89]
	v_mfma_f32_16x16x32_f16 v[90:93], v[26:29], v[204:207], v[90:93]
	v_mfma_f32_16x16x32_f16 v[94:97], v[30:33], v[204:207], v[94:97]
	s_setprio 0
	v_add_u32_e32 v192, 0x10000, v208
	v_add_u32_e32 v196, 0x14000, v208
	v_add_u32_e32 v200, 0x18000, v208
	v_add_u32_e32 v204, 0x1c000, v208
	ds_read_b128 v[192:195], v192
	ds_read_b128 v[196:199], v196
	ds_read_b128 v[200:203], v200
	ds_read_b128 v[204:207], v204
	s_setprio 1
	s_waitcnt lgkmcnt(3)
	v_mfma_f32_16x16x32_f16 v[98:101], v[18:21], v[192:195], v[98:101]
	v_mfma_f32_16x16x32_f16 v[102:105], v[22:25], v[192:195], v[102:105]
	v_mfma_f32_16x16x32_f16 v[106:109], v[26:29], v[192:195], v[106:109]
	v_mfma_f32_16x16x32_f16 v[110:113], v[30:33], v[192:195], v[110:113]
	s_waitcnt lgkmcnt(2)
	v_mfma_f32_16x16x32_f16 v[114:117], v[18:21], v[196:199], v[114:117]
	v_mfma_f32_16x16x32_f16 v[118:121], v[22:25], v[196:199], v[118:121]
	v_mfma_f32_16x16x32_f16 v[122:125], v[26:29], v[196:199], v[122:125]
	v_mfma_f32_16x16x32_f16 v[126:129], v[30:33], v[196:199], v[126:129]
	s_waitcnt lgkmcnt(1)
	v_mfma_f32_16x16x32_f16 v[130:133], v[18:21], v[200:203], v[130:133]
	v_mfma_f32_16x16x32_f16 v[134:137], v[22:25], v[200:203], v[134:137]
	v_mfma_f32_16x16x32_f16 v[138:141], v[26:29], v[200:203], v[138:141]
	s_waitcnt lgkmcnt(0)
	v_mfma_f32_16x16x32_f16 v[2:5], v[18:21], v[204:207], v[2:5]
	v_mfma_f32_16x16x32_f16 v[6:9], v[22:25], v[204:207], v[6:9]
	v_mfma_f32_16x16x32_f16 v[10:13], v[26:29], v[204:207], v[10:13]
	v_mfma_f32_16x16x32_f16 v[14:17], v[30:33], v[204:207], v[14:17]
	v_mfma_f32_16x16x32_f16 v[142:145], v[30:33], v[200:203], v[142:145]
	s_setprio 0
	s_xor_b32 s7, s51, 4
	s_lshl_b32 s0, s7, 12
	v_lshl_add_u64 v[30:31], v[166:167], 0, s[0:1]
	global_load_dwordx4 v[18:21], v[30:31], off
	global_load_dwordx4 v[22:25], v[30:31], off offset:1024
	global_load_dwordx4 v[26:29], v[30:31], off offset:2048
	s_nop 0
	global_load_dwordx4 v[30:33], v[30:31], off offset:3072
	v_lshl_add_u32 v208, s2, 10, v191
	ds_read_b128 v[192:195], v208
	ds_read_b128 v[196:199], v208 offset:16384
	ds_read_b128 v[200:203], v208 offset:32768
	ds_read_b128 v[204:207], v208 offset:49152
	s_setprio 1
	s_waitcnt vmcnt(11) lgkmcnt(3)
	v_mfma_f32_16x16x32_f16 v[34:37], v[162:165], v[192:195], v[34:37]
	s_waitcnt vmcnt(10)
	v_mfma_f32_16x16x32_f16 v[38:41], v[168:171], v[192:195], v[38:41]
	s_waitcnt vmcnt(9)
	v_mfma_f32_16x16x32_f16 v[42:45], v[172:175], v[192:195], v[42:45]
	s_waitcnt vmcnt(8)
	v_mfma_f32_16x16x32_f16 v[46:49], v[176:179], v[192:195], v[46:49]
	s_waitcnt lgkmcnt(2)
	v_mfma_f32_16x16x32_f16 v[50:53], v[162:165], v[196:199], v[50:53]
	v_mfma_f32_16x16x32_f16 v[54:57], v[168:171], v[196:199], v[54:57]
	v_mfma_f32_16x16x32_f16 v[58:61], v[172:175], v[196:199], v[58:61]
	v_mfma_f32_16x16x32_f16 v[62:65], v[176:179], v[196:199], v[62:65]
	s_waitcnt lgkmcnt(1)
	v_mfma_f32_16x16x32_f16 v[66:69], v[162:165], v[200:203], v[66:69]
	v_mfma_f32_16x16x32_f16 v[70:73], v[168:171], v[200:203], v[70:73]
	v_mfma_f32_16x16x32_f16 v[74:77], v[172:175], v[200:203], v[74:77]
	v_mfma_f32_16x16x32_f16 v[78:81], v[176:179], v[200:203], v[78:81]
	s_waitcnt lgkmcnt(0)
	v_mfma_f32_16x16x32_f16 v[82:85], v[162:165], v[204:207], v[82:85]
	v_mfma_f32_16x16x32_f16 v[86:89], v[168:171], v[204:207], v[86:89]
	v_mfma_f32_16x16x32_f16 v[90:93], v[172:175], v[204:207], v[90:93]
	v_mfma_f32_16x16x32_f16 v[94:97], v[176:179], v[204:207], v[94:97]
	s_setprio 0
	v_add_u32_e32 v192, 0x10000, v208
	v_add_u32_e32 v196, 0x14000, v208
	v_add_u32_e32 v200, 0x18000, v208
	v_add_u32_e32 v204, 0x1c000, v208
	ds_read_b128 v[192:195], v192
	ds_read_b128 v[196:199], v196
	ds_read_b128 v[200:203], v200
	ds_read_b128 v[204:207], v204
	s_setprio 1
	s_waitcnt lgkmcnt(3)
	v_mfma_f32_16x16x32_f16 v[98:101], v[162:165], v[192:195], v[98:101]
	v_mfma_f32_16x16x32_f16 v[102:105], v[168:171], v[192:195], v[102:105]
	v_mfma_f32_16x16x32_f16 v[106:109], v[172:175], v[192:195], v[106:109]
	v_mfma_f32_16x16x32_f16 v[110:113], v[176:179], v[192:195], v[110:113]
	s_waitcnt lgkmcnt(2)
	v_mfma_f32_16x16x32_f16 v[114:117], v[162:165], v[196:199], v[114:117]
	v_mfma_f32_16x16x32_f16 v[118:121], v[168:171], v[196:199], v[118:121]
	v_mfma_f32_16x16x32_f16 v[122:125], v[172:175], v[196:199], v[122:125]
	v_mfma_f32_16x16x32_f16 v[126:129], v[176:179], v[196:199], v[126:129]
	s_waitcnt lgkmcnt(1)
	v_mfma_f32_16x16x32_f16 v[130:133], v[162:165], v[200:203], v[130:133]
	v_mfma_f32_16x16x32_f16 v[134:137], v[168:171], v[200:203], v[134:137]
	v_mfma_f32_16x16x32_f16 v[138:141], v[172:175], v[200:203], v[138:141]
	s_waitcnt lgkmcnt(0)
	v_mfma_f32_16x16x32_f16 v[2:5], v[162:165], v[204:207], v[2:5]
	v_mfma_f32_16x16x32_f16 v[6:9], v[168:171], v[204:207], v[6:9]
	v_mfma_f32_16x16x32_f16 v[10:13], v[172:175], v[204:207], v[10:13]
	v_mfma_f32_16x16x32_f16 v[14:17], v[176:179], v[204:207], v[14:17]
	v_mfma_f32_16x16x32_f16 v[142:145], v[176:179], v[200:203], v[142:145]
	s_setprio 0
	s_or_b32 s2, s49, s30
	s_lshl_b32 s0, s2, 12
	v_lshl_add_u64 v[176:177], v[166:167], 0, s[0:1]
	global_load_dwordx4 v[162:165], v[176:177], off
	global_load_dwordx4 v[168:171], v[176:177], off offset:1024
	global_load_dwordx4 v[172:175], v[176:177], off offset:2048
	s_nop 0
	global_load_dwordx4 v[176:179], v[176:177], off offset:3072
	v_lshl_add_u32 v208, s3, 10, v191
	ds_read_b128 v[192:195], v208
	ds_read_b128 v[196:199], v208 offset:16384
	ds_read_b128 v[200:203], v208 offset:32768
	ds_read_b128 v[204:207], v208 offset:49152
	s_setprio 1
	s_waitcnt vmcnt(11) lgkmcnt(3)
	v_mfma_f32_16x16x32_f16 v[34:37], v[146:149], v[192:195], v[34:37]
	s_waitcnt vmcnt(10)
	v_mfma_f32_16x16x32_f16 v[38:41], v[150:153], v[192:195], v[38:41]
	s_waitcnt vmcnt(9)
	v_mfma_f32_16x16x32_f16 v[42:45], v[154:157], v[192:195], v[42:45]
	s_waitcnt vmcnt(8)
	v_mfma_f32_16x16x32_f16 v[46:49], v[158:161], v[192:195], v[46:49]
	s_waitcnt lgkmcnt(2)
	v_mfma_f32_16x16x32_f16 v[50:53], v[146:149], v[196:199], v[50:53]
	v_mfma_f32_16x16x32_f16 v[54:57], v[150:153], v[196:199], v[54:57]
	v_mfma_f32_16x16x32_f16 v[58:61], v[154:157], v[196:199], v[58:61]
	v_mfma_f32_16x16x32_f16 v[62:65], v[158:161], v[196:199], v[62:65]
	s_waitcnt lgkmcnt(1)
	v_mfma_f32_16x16x32_f16 v[66:69], v[146:149], v[200:203], v[66:69]
	v_mfma_f32_16x16x32_f16 v[70:73], v[150:153], v[200:203], v[70:73]
	v_mfma_f32_16x16x32_f16 v[74:77], v[154:157], v[200:203], v[74:77]
	v_mfma_f32_16x16x32_f16 v[78:81], v[158:161], v[200:203], v[78:81]
	s_waitcnt lgkmcnt(0)
	v_mfma_f32_16x16x32_f16 v[82:85], v[146:149], v[204:207], v[82:85]
	v_mfma_f32_16x16x32_f16 v[86:89], v[150:153], v[204:207], v[86:89]
	v_mfma_f32_16x16x32_f16 v[90:93], v[154:157], v[204:207], v[90:93]
	v_mfma_f32_16x16x32_f16 v[94:97], v[158:161], v[204:207], v[94:97]
	s_setprio 0
	v_add_u32_e32 v192, 0x10000, v208
	v_add_u32_e32 v196, 0x14000, v208
	v_add_u32_e32 v200, 0x18000, v208
	v_add_u32_e32 v204, 0x1c000, v208
	ds_read_b128 v[192:195], v192
	ds_read_b128 v[196:199], v196
	ds_read_b128 v[200:203], v200
	ds_read_b128 v[204:207], v204
	s_setprio 1
	s_waitcnt lgkmcnt(3)
	v_mfma_f32_16x16x32_f16 v[98:101], v[146:149], v[192:195], v[98:101]
	v_mfma_f32_16x16x32_f16 v[102:105], v[150:153], v[192:195], v[102:105]
	v_mfma_f32_16x16x32_f16 v[106:109], v[154:157], v[192:195], v[106:109]
	v_mfma_f32_16x16x32_f16 v[110:113], v[158:161], v[192:195], v[110:113]
	s_waitcnt lgkmcnt(2)
	v_mfma_f32_16x16x32_f16 v[114:117], v[146:149], v[196:199], v[114:117]
	v_mfma_f32_16x16x32_f16 v[118:121], v[150:153], v[196:199], v[118:121]
	v_mfma_f32_16x16x32_f16 v[122:125], v[154:157], v[196:199], v[122:125]
	v_mfma_f32_16x16x32_f16 v[126:129], v[158:161], v[196:199], v[126:129]
	s_waitcnt lgkmcnt(1)
	v_mfma_f32_16x16x32_f16 v[130:133], v[146:149], v[200:203], v[130:133]
	v_mfma_f32_16x16x32_f16 v[134:137], v[150:153], v[200:203], v[134:137]
	v_mfma_f32_16x16x32_f16 v[138:141], v[154:157], v[200:203], v[138:141]
	s_waitcnt lgkmcnt(0)
	v_mfma_f32_16x16x32_f16 v[2:5], v[146:149], v[204:207], v[2:5]
	v_mfma_f32_16x16x32_f16 v[6:9], v[150:153], v[204:207], v[6:9]
	v_mfma_f32_16x16x32_f16 v[10:13], v[154:157], v[204:207], v[10:13]
	v_mfma_f32_16x16x32_f16 v[14:17], v[158:161], v[204:207], v[14:17]
	v_mfma_f32_16x16x32_f16 v[142:145], v[158:161], v[200:203], v[142:145]
	s_setprio 0
	s_or_b32 s3, s49, s31
	s_lshl_b32 s0, s3, 12
	v_lshl_add_u64 v[158:159], v[166:167], 0, s[0:1]
	global_load_dwordx4 v[146:149], v[158:159], off
	global_load_dwordx4 v[150:153], v[158:159], off offset:1024
	global_load_dwordx4 v[154:157], v[158:159], off offset:2048
	s_nop 0
	global_load_dwordx4 v[158:161], v[158:159], off offset:3072
	v_lshl_add_u32 v208, s7, 10, v191
	ds_read_b128 v[192:195], v208
	ds_read_b128 v[196:199], v208 offset:16384
	ds_read_b128 v[200:203], v208 offset:32768
	ds_read_b128 v[204:207], v208 offset:49152
	s_setprio 1
	s_waitcnt vmcnt(11) lgkmcnt(3)
	v_mfma_f32_16x16x32_f16 v[34:37], v[18:21], v[192:195], v[34:37]
	s_waitcnt vmcnt(10)
	v_mfma_f32_16x16x32_f16 v[38:41], v[22:25], v[192:195], v[38:41]
	s_waitcnt vmcnt(9)
	v_mfma_f32_16x16x32_f16 v[42:45], v[26:29], v[192:195], v[42:45]
	s_waitcnt vmcnt(8)
	v_mfma_f32_16x16x32_f16 v[46:49], v[30:33], v[192:195], v[46:49]
	s_waitcnt lgkmcnt(2)
	v_mfma_f32_16x16x32_f16 v[50:53], v[18:21], v[196:199], v[50:53]
	v_mfma_f32_16x16x32_f16 v[54:57], v[22:25], v[196:199], v[54:57]
	v_mfma_f32_16x16x32_f16 v[58:61], v[26:29], v[196:199], v[58:61]
	v_mfma_f32_16x16x32_f16 v[62:65], v[30:33], v[196:199], v[62:65]
	s_waitcnt lgkmcnt(1)
	v_mfma_f32_16x16x32_f16 v[66:69], v[18:21], v[200:203], v[66:69]
	v_mfma_f32_16x16x32_f16 v[70:73], v[22:25], v[200:203], v[70:73]
	v_mfma_f32_16x16x32_f16 v[74:77], v[26:29], v[200:203], v[74:77]
	v_mfma_f32_16x16x32_f16 v[78:81], v[30:33], v[200:203], v[78:81]
	s_waitcnt lgkmcnt(0)
	v_mfma_f32_16x16x32_f16 v[82:85], v[18:21], v[204:207], v[82:85]
	v_mfma_f32_16x16x32_f16 v[86:89], v[22:25], v[204:207], v[86:89]
	v_mfma_f32_16x16x32_f16 v[90:93], v[26:29], v[204:207], v[90:93]
	v_mfma_f32_16x16x32_f16 v[94:97], v[30:33], v[204:207], v[94:97]
	s_setprio 0
	v_add_u32_e32 v192, 0x10000, v208
	v_add_u32_e32 v196, 0x14000, v208
	v_add_u32_e32 v200, 0x18000, v208
	v_add_u32_e32 v204, 0x1c000, v208
	ds_read_b128 v[192:195], v192
	ds_read_b128 v[196:199], v196
	ds_read_b128 v[200:203], v200
	ds_read_b128 v[204:207], v204
	s_setprio 1
	s_waitcnt lgkmcnt(3)
	v_mfma_f32_16x16x32_f16 v[98:101], v[18:21], v[192:195], v[98:101]
	v_mfma_f32_16x16x32_f16 v[102:105], v[22:25], v[192:195], v[102:105]
	v_mfma_f32_16x16x32_f16 v[106:109], v[26:29], v[192:195], v[106:109]
	v_mfma_f32_16x16x32_f16 v[110:113], v[30:33], v[192:195], v[110:113]
	s_waitcnt lgkmcnt(2)
	v_mfma_f32_16x16x32_f16 v[114:117], v[18:21], v[196:199], v[114:117]
	v_mfma_f32_16x16x32_f16 v[118:121], v[22:25], v[196:199], v[118:121]
	v_mfma_f32_16x16x32_f16 v[122:125], v[26:29], v[196:199], v[122:125]
	v_mfma_f32_16x16x32_f16 v[126:129], v[30:33], v[196:199], v[126:129]
	s_waitcnt lgkmcnt(1)
	v_mfma_f32_16x16x32_f16 v[130:133], v[18:21], v[200:203], v[130:133]
	v_mfma_f32_16x16x32_f16 v[134:137], v[22:25], v[200:203], v[134:137]
	v_mfma_f32_16x16x32_f16 v[138:141], v[26:29], v[200:203], v[138:141]
	s_waitcnt lgkmcnt(0)
	v_mfma_f32_16x16x32_f16 v[2:5], v[18:21], v[204:207], v[2:5]
	v_mfma_f32_16x16x32_f16 v[6:9], v[22:25], v[204:207], v[6:9]
	v_mfma_f32_16x16x32_f16 v[10:13], v[26:29], v[204:207], v[10:13]
	v_mfma_f32_16x16x32_f16 v[14:17], v[30:33], v[204:207], v[14:17]
	v_mfma_f32_16x16x32_f16 v[142:145], v[30:33], v[200:203], v[142:145]
	s_setprio 0
	s_or_b32 s7, s49, s48
	s_lshl_b32 s0, s7, 12
	v_lshl_add_u64 v[26:27], v[166:167], 0, s[0:1]
	global_load_dwordx4 v[18:21], v[26:27], off
	global_load_dwordx4 v[22:25], v[26:27], off offset:1024
	global_load_dwordx4 v[30:33], v[26:27], off offset:2048
	global_load_dwordx4 v[192:195], v[26:27], off offset:3072
	v_lshl_add_u32 v166, s2, 10, v191
	ds_read_b128 v[26:29], v166
	ds_read_b128 v[196:199], v166 offset:16384
	ds_read_b128 v[200:203], v166 offset:32768
	ds_read_b128 v[204:207], v166 offset:49152
	s_setprio 1
	s_waitcnt vmcnt(11) lgkmcnt(3)
	v_mfma_f32_16x16x32_f16 v[34:37], v[162:165], v[26:29], v[34:37]
	s_waitcnt vmcnt(10)
	v_mfma_f32_16x16x32_f16 v[38:41], v[168:171], v[26:29], v[38:41]
	s_waitcnt vmcnt(9)
	v_mfma_f32_16x16x32_f16 v[42:45], v[172:175], v[26:29], v[42:45]
	s_waitcnt vmcnt(8)
	v_mfma_f32_16x16x32_f16 v[26:29], v[176:179], v[26:29], v[46:49]
	s_waitcnt lgkmcnt(2)
	v_mfma_f32_16x16x32_f16 v[46:49], v[162:165], v[196:199], v[50:53]
	v_mfma_f32_16x16x32_f16 v[50:53], v[168:171], v[196:199], v[54:57]
	v_mfma_f32_16x16x32_f16 v[54:57], v[172:175], v[196:199], v[58:61]
	v_mfma_f32_16x16x32_f16 v[58:61], v[176:179], v[196:199], v[62:65]
	s_waitcnt lgkmcnt(1)
	v_mfma_f32_16x16x32_f16 v[62:65], v[162:165], v[200:203], v[66:69]
	v_mfma_f32_16x16x32_f16 v[66:69], v[168:171], v[200:203], v[70:73]
	v_mfma_f32_16x16x32_f16 v[70:73], v[172:175], v[200:203], v[74:77]
	v_mfma_f32_16x16x32_f16 v[74:77], v[176:179], v[200:203], v[78:81]
	s_waitcnt lgkmcnt(0)
	v_mfma_f32_16x16x32_f16 v[78:81], v[162:165], v[204:207], v[82:85]
	v_mfma_f32_16x16x32_f16 v[82:85], v[168:171], v[204:207], v[86:89]
	v_mfma_f32_16x16x32_f16 v[86:89], v[172:175], v[204:207], v[90:93]
	v_mfma_f32_16x16x32_f16 v[90:93], v[176:179], v[204:207], v[94:97]
	s_setprio 0
	s_nop 1
	v_add_u32_e32 v94, 0x10000, v166
	v_add_u32_e32 v167, 0x14000, v166
	ds_read_b128 v[94:97], v94
	ds_read_b128 v[196:199], v167
	v_add_u32_e32 v167, 0x18000, v166
	v_add_u32_e32 v166, 0x1c000, v166
	ds_read_b128 v[200:203], v167
	ds_read_b128 v[204:207], v166
	s_setprio 1
	s_waitcnt lgkmcnt(3)
	v_mfma_f32_16x16x32_f16 v[98:101], v[162:165], v[94:97], v[98:101]
	v_mfma_f32_16x16x32_f16 v[102:105], v[168:171], v[94:97], v[102:105]
	v_mfma_f32_16x16x32_f16 v[106:109], v[172:175], v[94:97], v[106:109]
	v_mfma_f32_16x16x32_f16 v[94:97], v[176:179], v[94:97], v[110:113]
	s_waitcnt lgkmcnt(2)
	v_mfma_f32_16x16x32_f16 v[110:113], v[162:165], v[196:199], v[114:117]
	v_mfma_f32_16x16x32_f16 v[114:117], v[168:171], v[196:199], v[118:121]
	v_mfma_f32_16x16x32_f16 v[118:121], v[172:175], v[196:199], v[122:125]
	v_mfma_f32_16x16x32_f16 v[122:125], v[176:179], v[196:199], v[126:129]
	s_waitcnt lgkmcnt(1)
	v_mfma_f32_16x16x32_f16 v[126:129], v[162:165], v[200:203], v[130:133]
	v_mfma_f32_16x16x32_f16 v[130:133], v[168:171], v[200:203], v[134:137]
	v_mfma_f32_16x16x32_f16 v[134:137], v[172:175], v[200:203], v[138:141]
	v_mfma_f32_16x16x32_f16 v[138:141], v[176:179], v[200:203], v[142:145]
	s_waitcnt lgkmcnt(0)
	v_mfma_f32_16x16x32_f16 v[2:5], v[162:165], v[204:207], v[2:5]
	v_mfma_f32_16x16x32_f16 v[6:9], v[168:171], v[204:207], v[6:9]
	v_mfma_f32_16x16x32_f16 v[10:13], v[172:175], v[204:207], v[10:13]
	v_mfma_f32_16x16x32_f16 v[14:17], v[176:179], v[204:207], v[14:17]
	s_setprio 0
	v_lshl_add_u32 v174, s3, 10, v191
	ds_read_b128 v[142:145], v174
	ds_read_b128 v[162:165], v174 offset:16384
	ds_read_b128 v[166:169], v174 offset:32768
	ds_read_b128 v[170:173], v174 offset:49152
	s_setprio 1
	s_waitcnt vmcnt(7) lgkmcnt(3)
	v_mfma_f32_16x16x32_f16 v[34:37], v[146:149], v[142:145], v[34:37]
	s_waitcnt vmcnt(6)
	v_mfma_f32_16x16x32_f16 v[38:41], v[150:153], v[142:145], v[38:41]
	s_waitcnt vmcnt(5)
	v_mfma_f32_16x16x32_f16 v[42:45], v[154:157], v[142:145], v[42:45]
	s_waitcnt vmcnt(4)
	v_mfma_f32_16x16x32_f16 v[26:29], v[158:161], v[142:145], v[26:29]
	s_waitcnt lgkmcnt(2)
	v_mfma_f32_16x16x32_f16 v[46:49], v[146:149], v[162:165], v[46:49]
	v_mfma_f32_16x16x32_f16 v[50:53], v[150:153], v[162:165], v[50:53]
	v_mfma_f32_16x16x32_f16 v[54:57], v[154:157], v[162:165], v[54:57]
	v_mfma_f32_16x16x32_f16 v[58:61], v[158:161], v[162:165], v[58:61]
	s_waitcnt lgkmcnt(1)
	v_mfma_f32_16x16x32_f16 v[62:65], v[146:149], v[166:169], v[62:65]
	v_mfma_f32_16x16x32_f16 v[66:69], v[150:153], v[166:169], v[66:69]
	v_mfma_f32_16x16x32_f16 v[70:73], v[154:157], v[166:169], v[70:73]
	v_mfma_f32_16x16x32_f16 v[74:77], v[158:161], v[166:169], v[74:77]
	s_waitcnt lgkmcnt(0)
	v_mfma_f32_16x16x32_f16 v[78:81], v[146:149], v[170:173], v[78:81]
	v_mfma_f32_16x16x32_f16 v[82:85], v[150:153], v[170:173], v[82:85]
	v_mfma_f32_16x16x32_f16 v[86:89], v[154:157], v[170:173], v[86:89]
	v_mfma_f32_16x16x32_f16 v[162:165], v[158:161], v[170:173], v[90:93]
	s_setprio 0
	s_nop 1
	v_add_u32_e32 v90, 0x10000, v174
	v_add_u32_e32 v142, 0x14000, v174
	v_add_u32_e32 v166, 0x18000, v174
	v_add_u32_e32 v170, 0x1c000, v174
	ds_read_b128 v[90:93], v90
	ds_read_b128 v[142:145], v142
	ds_read_b128 v[166:169], v166
	ds_read_b128 v[170:173], v170
	s_setprio 1
	s_waitcnt lgkmcnt(0)
	v_mfma_f32_16x16x32_f16 v[2:5], v[146:149], v[170:173], v[2:5]
	v_mfma_f32_16x16x32_f16 v[6:9], v[150:153], v[170:173], v[6:9]
	v_mfma_f32_16x16x32_f16 v[10:13], v[154:157], v[170:173], v[10:13]
	v_mfma_f32_16x16x32_f16 v[14:17], v[158:161], v[170:173], v[14:17]
	v_mfma_f32_16x16x32_f16 v[174:177], v[146:149], v[90:93], v[98:101]
	v_mfma_f32_16x16x32_f16 v[196:199], v[150:153], v[90:93], v[102:105]
	v_mfma_f32_16x16x32_f16 v[200:203], v[154:157], v[90:93], v[106:109]
	v_mfma_f32_16x16x32_f16 v[204:207], v[158:161], v[90:93], v[94:97]
	v_mfma_f32_16x16x32_f16 v[208:211], v[146:149], v[142:145], v[110:113]
	v_mfma_f32_16x16x32_f16 v[212:215], v[150:153], v[142:145], v[114:117]
	v_mfma_f32_16x16x32_f16 v[216:219], v[154:157], v[142:145], v[118:121]
	v_mfma_f32_16x16x32_f16 v[220:223], v[158:161], v[142:145], v[122:125]
	v_mfma_f32_16x16x32_f16 v[224:227], v[146:149], v[166:169], v[126:129]
	v_mfma_f32_16x16x32_f16 v[228:231], v[150:153], v[166:169], v[130:133]
	v_mfma_f32_16x16x32_f16 v[232:235], v[154:157], v[166:169], v[134:137]
	v_mfma_f32_16x16x32_f16 v[166:169], v[158:161], v[166:169], v[138:141]
	s_setprio 0
	v_lshl_add_u32 v158, s7, 10, v191
	ds_read_b128 v[90:93], v158
	ds_read_b128 v[94:97], v158 offset:16384
	ds_read_b128 v[98:101], v158 offset:32768
	ds_read_b128 v[146:149], v158 offset:49152
	s_setprio 1
	s_waitcnt vmcnt(3) lgkmcnt(3)
	v_mfma_f32_16x16x32_f16 v[150:153], v[18:21], v[90:93], v[34:37]
	s_waitcnt vmcnt(2)
	v_mfma_f32_16x16x32_f16 v[138:141], v[22:25], v[90:93], v[38:41]
	s_waitcnt vmcnt(1)
	v_mfma_f32_16x16x32_f16 v[154:157], v[30:33], v[90:93], v[42:45]
	s_waitcnt vmcnt(0)
	v_mfma_f32_16x16x32_f16 v[142:145], v[192:195], v[90:93], v[26:29]
	s_waitcnt lgkmcnt(2)
	v_mfma_f32_16x16x32_f16 v[134:137], v[18:21], v[94:97], v[46:49]
	v_mfma_f32_16x16x32_f16 v[122:125], v[22:25], v[94:97], v[50:53]
	v_mfma_f32_16x16x32_f16 v[130:133], v[30:33], v[94:97], v[54:57]
	v_mfma_f32_16x16x32_f16 v[126:129], v[192:195], v[94:97], v[58:61]
	s_waitcnt lgkmcnt(1)
	v_mfma_f32_16x16x32_f16 v[118:121], v[18:21], v[98:101], v[62:65]
	v_mfma_f32_16x16x32_f16 v[106:109], v[22:25], v[98:101], v[66:69]
	v_mfma_f32_16x16x32_f16 v[114:117], v[30:33], v[98:101], v[70:73]
	v_mfma_f32_16x16x32_f16 v[110:113], v[192:195], v[98:101], v[74:77]
	s_waitcnt lgkmcnt(0)
	v_mfma_f32_16x16x32_f16 v[102:105], v[18:21], v[146:149], v[78:81]
	v_mfma_f32_16x16x32_f16 v[90:93], v[22:25], v[146:149], v[82:85]
	v_mfma_f32_16x16x32_f16 v[98:101], v[30:33], v[146:149], v[86:89]
	v_mfma_f32_16x16x32_f16 v[94:97], v[192:195], v[146:149], v[162:165]
	s_setprio 0
	v_add_u32_e32 v26, 0x10000, v158
	v_add_u32_e32 v34, 0x14000, v158
	v_add_u32_e32 v38, 0x18000, v158
	ds_read_b128 v[26:29], v26
	ds_read_b128 v[34:37], v34
	v_add_u32_e32 v42, 0x1c000, v158
	ds_read_b128 v[38:41], v38
	ds_read_b128 v[146:149], v42
	s_setprio 1
	s_waitcnt lgkmcnt(3)
	v_mfma_f32_16x16x32_f16 v[86:89], v[18:21], v[26:29], v[174:177]
	v_mfma_f32_16x16x32_f16 v[74:77], v[22:25], v[26:29], v[196:199]
	v_mfma_f32_16x16x32_f16 v[82:85], v[30:33], v[26:29], v[200:203]
	v_mfma_f32_16x16x32_f16 v[78:81], v[192:195], v[26:29], v[204:207]
	s_waitcnt lgkmcnt(2)
	v_mfma_f32_16x16x32_f16 v[70:73], v[18:21], v[34:37], v[208:211]
	v_mfma_f32_16x16x32_f16 v[58:61], v[22:25], v[34:37], v[212:215]
	v_mfma_f32_16x16x32_f16 v[66:69], v[30:33], v[34:37], v[216:219]
	v_mfma_f32_16x16x32_f16 v[62:65], v[192:195], v[34:37], v[220:223]
	s_waitcnt lgkmcnt(1)
	v_mfma_f32_16x16x32_f16 v[54:57], v[18:21], v[38:41], v[224:227]
	v_mfma_f32_16x16x32_f16 v[42:45], v[22:25], v[38:41], v[228:231]
	v_mfma_f32_16x16x32_f16 v[50:53], v[30:33], v[38:41], v[232:235]
	v_mfma_f32_16x16x32_f16 v[46:49], v[192:195], v[38:41], v[166:169]
	s_waitcnt lgkmcnt(0)
	v_mfma_f32_16x16x32_f16 v[26:29], v[18:21], v[146:149], v[2:5]
	v_mfma_f32_16x16x32_f16 v[2:5], v[22:25], v[146:149], v[6:9]
	v_mfma_f32_16x16x32_f16 v[22:25], v[30:33], v[146:149], v[10:13]
	v_mfma_f32_16x16x32_f16 v[6:9], v[192:195], v[146:149], v[14:17]
	s_setprio 0
	s_lshl_b64 s[0:1], s[42:43], 2
	s_add_u32 s0, s18, s0
	s_addc_u32 s1, s19, s1
	s_lshl_b32 s2, s42, 8
	s_ashr_i32 s3, s2, 31
	v_lshlrev_b32_e32 v146, 5, v187
	s_lshl_b64 s[2:3], s[2:3], 2
	v_and_or_b32 v10, v190, 12, v146
	s_add_u32 s12, s12, s2
	s_addc_u32 s13, s13, s3
	v_lshlrev_b32_e32 v10, 2, v10
	v_add_u32_e32 v254, 0x22640, v10
	ds_read_b128 v[34:37], v254
	ds_read_b128 v[14:17], v254 offset:64
	ds_read_b128 v[38:41], v254 offset:1024
	ds_read_b128 v[18:21], v254 offset:1088
	ds_read_b128 v[30:33], v254 offset:2048
	ds_read_b128 v[10:13], v254 offset:2112
	s_add_u32 s12, s14, s2
	s_addc_u32 s13, s15, s3
	s_add_u32 s2, s16, s2
	s_addc_u32 s3, s17, s3
	s_nop 0
	v_cmp_gt_u32_e32 vcc, 16, v189
	s_mov_b32 s2, s69
	v_mov_b32_e32 v216, 0x3d38aa3b
	v_mov_b32_e32 v217, 0x3d38aa3b
	v_mov_b32_e32 v218, 0xbcb8aa3b
	v_mov_b32_e32 v219, 0xbcb8aa3b
	v_mov_b32_e32 v222, 1.0
	v_mov_b32_e32 v223, 1.0
	v_mov_b32_e32 v224, 0x4038aa3b
	v_mov_b32_e32 v225, 0x4038aa3b
	v_mov_b32_e32 v226, 0xbfb8aa3b
	v_mov_b32_e32 v227, 0xbfb8aa3b
	v_lshlrev_b32_e32 v232, 9, v187
	v_lshlrev_b32_e32 v233, 2, v188
	v_add3_u32 v232, s24, v232, v233
	s_waitcnt vmcnt(0) lgkmcnt(0)
	v_pk_mul_f32 v[34:35], v[34:35], v[224:225]
	v_pk_mul_f32 v[36:37], v[36:37], v[224:225]
	v_pk_mul_f32 v[14:15], v[14:15], v[224:225]
	v_pk_mul_f32 v[16:17], v[16:17], v[224:225]
	v_pk_mul_f32 v[38:39], v[38:39], v[226:227]
	v_pk_mul_f32 v[40:41], v[40:41], v[226:227]
	v_pk_mul_f32 v[18:19], v[18:19], v[226:227]
	v_pk_mul_f32 v[20:21], v[20:21], v[226:227]
	v_pk_fma_f32 v[150:151], v[150:151], v[216:217], v[34:35]
	v_pk_fma_f32 v[154:155], v[154:155], v[218:219], v[38:39]
	v_min_f32_e32 v150, 0x42700000, v150
	v_min_f32_e32 v151, 0x42700000, v151
	v_min_f32_e32 v154, 0x42700000, v154
	v_min_f32_e32 v155, 0x42700000, v155
	v_pk_fma_f32 v[152:153], v[152:153], v[216:217], v[36:37]
	v_pk_fma_f32 v[156:157], v[156:157], v[218:219], v[40:41]
	v_min_f32_e32 v152, 0x42700000, v152
	v_min_f32_e32 v153, 0x42700000, v153
	v_min_f32_e32 v156, 0x42700000, v156
	v_min_f32_e32 v157, 0x42700000, v157
	v_exp_f32_e32 v150, v150
	v_exp_f32_e32 v151, v151
	v_exp_f32_e32 v154, v154
	v_exp_f32_e32 v155, v155
	v_exp_f32_e32 v152, v152
	v_exp_f32_e32 v153, v153
	v_exp_f32_e32 v156, v156
	v_exp_f32_e32 v157, v157
	v_pk_fma_f32 v[228:229], v[150:151], v[30:31], v[30:31] neg_lo:[0,0,1] neg_hi:[0,0,1]
	v_pk_add_f32 v[154:155], v[154:155], v[222:223]
	v_pk_fma_f32 v[150:151], v[150:151], v[154:155], v[154:155]
	v_pk_fma_f32 v[230:231], v[152:153], v[32:33], v[32:33] neg_lo:[0,0,1] neg_hi:[0,0,1]
	v_pk_add_f32 v[156:157], v[156:157], v[222:223]
	v_pk_fma_f32 v[152:153], v[152:153], v[156:157], v[156:157]
	v_rcp_f32_e32 v150, v150
	v_rcp_f32_e32 v151, v151
	v_rcp_f32_e32 v152, v152
	v_rcp_f32_e32 v153, v153
	v_pk_mul_f32 v[200:201], v[228:229], v[150:151]
	v_pk_fma_f32 v[200:201], v[230:231], v[152:153], v[200:201]
	v_pk_fma_f32 v[138:139], v[138:139], v[216:217], v[14:15]
	v_pk_fma_f32 v[142:143], v[142:143], v[218:219], v[18:19]
	v_min_f32_e32 v138, 0x42700000, v138
	v_min_f32_e32 v139, 0x42700000, v139
	v_min_f32_e32 v142, 0x42700000, v142
	v_min_f32_e32 v143, 0x42700000, v143
	v_pk_fma_f32 v[140:141], v[140:141], v[216:217], v[16:17]
	v_pk_fma_f32 v[144:145], v[144:145], v[218:219], v[20:21]
	v_min_f32_e32 v140, 0x42700000, v140
	v_min_f32_e32 v141, 0x42700000, v141
	v_min_f32_e32 v144, 0x42700000, v144
	v_min_f32_e32 v145, 0x42700000, v145
	v_exp_f32_e32 v138, v138
	v_exp_f32_e32 v139, v139
	v_exp_f32_e32 v142, v142
	v_exp_f32_e32 v143, v143
	v_exp_f32_e32 v140, v140
	v_exp_f32_e32 v141, v141
	v_exp_f32_e32 v144, v144
	v_exp_f32_e32 v145, v145
	v_pk_fma_f32 v[228:229], v[138:139], v[10:11], v[10:11] neg_lo:[0,0,1] neg_hi:[0,0,1]
	v_pk_add_f32 v[142:143], v[142:143], v[222:223]
	v_pk_fma_f32 v[138:139], v[138:139], v[142:143], v[142:143]
	v_pk_fma_f32 v[230:231], v[140:141], v[12:13], v[12:13] neg_lo:[0,0,1] neg_hi:[0,0,1]
	v_pk_add_f32 v[144:145], v[144:145], v[222:223]
	v_pk_fma_f32 v[140:141], v[140:141], v[144:145], v[144:145]
	v_rcp_f32_e32 v138, v138
	v_rcp_f32_e32 v139, v139
	v_rcp_f32_e32 v140, v140
	v_rcp_f32_e32 v141, v141
	v_pk_fma_f32 v[200:201], v[228:229], v[138:139], v[200:201]
	v_pk_fma_f32 v[200:201], v[230:231], v[140:141], v[200:201]
	v_pk_fma_f32 v[134:135], v[134:135], v[216:217], v[34:35]
	v_pk_fma_f32 v[130:131], v[130:131], v[218:219], v[38:39]
	v_min_f32_e32 v134, 0x42700000, v134
	v_min_f32_e32 v135, 0x42700000, v135
	v_min_f32_e32 v130, 0x42700000, v130
	v_min_f32_e32 v131, 0x42700000, v131
	v_pk_fma_f32 v[136:137], v[136:137], v[216:217], v[36:37]
	v_pk_fma_f32 v[132:133], v[132:133], v[218:219], v[40:41]
	v_min_f32_e32 v136, 0x42700000, v136
	v_min_f32_e32 v137, 0x42700000, v137
	v_min_f32_e32 v132, 0x42700000, v132
	v_min_f32_e32 v133, 0x42700000, v133
	v_exp_f32_e32 v134, v134
	v_exp_f32_e32 v135, v135
	v_exp_f32_e32 v130, v130
	v_exp_f32_e32 v131, v131
	v_exp_f32_e32 v136, v136
	v_exp_f32_e32 v137, v137
	v_exp_f32_e32 v132, v132
	v_exp_f32_e32 v133, v133
	v_pk_fma_f32 v[228:229], v[134:135], v[30:31], v[30:31] neg_lo:[0,0,1] neg_hi:[0,0,1]
	v_pk_add_f32 v[130:131], v[130:131], v[222:223]
	v_pk_fma_f32 v[134:135], v[134:135], v[130:131], v[130:131]
	v_pk_fma_f32 v[230:231], v[136:137], v[32:33], v[32:33] neg_lo:[0,0,1] neg_hi:[0,0,1]
	v_pk_add_f32 v[132:133], v[132:133], v[222:223]
	v_pk_fma_f32 v[136:137], v[136:137], v[132:133], v[132:133]
	v_rcp_f32_e32 v134, v134
	v_rcp_f32_e32 v135, v135
	v_rcp_f32_e32 v136, v136
	v_rcp_f32_e32 v137, v137
	v_pk_mul_f32 v[202:203], v[228:229], v[134:135]
	v_pk_fma_f32 v[202:203], v[230:231], v[136:137], v[202:203]
	v_pk_fma_f32 v[122:123], v[122:123], v[216:217], v[14:15]
	v_pk_fma_f32 v[126:127], v[126:127], v[218:219], v[18:19]
	v_min_f32_e32 v122, 0x42700000, v122
	v_min_f32_e32 v123, 0x42700000, v123
	v_min_f32_e32 v126, 0x42700000, v126
	v_min_f32_e32 v127, 0x42700000, v127
	v_pk_fma_f32 v[124:125], v[124:125], v[216:217], v[16:17]
	v_pk_fma_f32 v[128:129], v[128:129], v[218:219], v[20:21]
	v_min_f32_e32 v124, 0x42700000, v124
	v_min_f32_e32 v125, 0x42700000, v125
	v_min_f32_e32 v128, 0x42700000, v128
	v_min_f32_e32 v129, 0x42700000, v129
	v_exp_f32_e32 v122, v122
	v_exp_f32_e32 v123, v123
	v_exp_f32_e32 v126, v126
	v_exp_f32_e32 v127, v127
	v_exp_f32_e32 v124, v124
	v_exp_f32_e32 v125, v125
	v_exp_f32_e32 v128, v128
	v_exp_f32_e32 v129, v129
	v_pk_fma_f32 v[228:229], v[122:123], v[10:11], v[10:11] neg_lo:[0,0,1] neg_hi:[0,0,1]
	v_pk_add_f32 v[126:127], v[126:127], v[222:223]
	v_pk_fma_f32 v[122:123], v[122:123], v[126:127], v[126:127]
	v_pk_fma_f32 v[230:231], v[124:125], v[12:13], v[12:13] neg_lo:[0,0,1] neg_hi:[0,0,1]
	v_pk_add_f32 v[128:129], v[128:129], v[222:223]
	v_pk_fma_f32 v[124:125], v[124:125], v[128:129], v[128:129]
	v_rcp_f32_e32 v122, v122
	v_rcp_f32_e32 v123, v123
	v_rcp_f32_e32 v124, v124
	v_rcp_f32_e32 v125, v125
	v_pk_fma_f32 v[202:203], v[228:229], v[122:123], v[202:203]
	v_pk_fma_f32 v[202:203], v[230:231], v[124:125], v[202:203]
	v_pk_fma_f32 v[118:119], v[118:119], v[216:217], v[34:35]
	v_pk_fma_f32 v[114:115], v[114:115], v[218:219], v[38:39]
	v_min_f32_e32 v118, 0x42700000, v118
	v_min_f32_e32 v119, 0x42700000, v119
	v_min_f32_e32 v114, 0x42700000, v114
	v_min_f32_e32 v115, 0x42700000, v115
	v_pk_fma_f32 v[120:121], v[120:121], v[216:217], v[36:37]
	v_pk_fma_f32 v[116:117], v[116:117], v[218:219], v[40:41]
	v_min_f32_e32 v120, 0x42700000, v120
	v_min_f32_e32 v121, 0x42700000, v121
	v_min_f32_e32 v116, 0x42700000, v116
	v_min_f32_e32 v117, 0x42700000, v117
	v_exp_f32_e32 v118, v118
	v_exp_f32_e32 v119, v119
	v_exp_f32_e32 v114, v114
	v_exp_f32_e32 v115, v115
	v_exp_f32_e32 v120, v120
	v_exp_f32_e32 v121, v121
	v_exp_f32_e32 v116, v116
	v_exp_f32_e32 v117, v117
	v_pk_fma_f32 v[228:229], v[118:119], v[30:31], v[30:31] neg_lo:[0,0,1] neg_hi:[0,0,1]
	v_pk_add_f32 v[114:115], v[114:115], v[222:223]
	v_pk_fma_f32 v[118:119], v[118:119], v[114:115], v[114:115]
	v_pk_fma_f32 v[230:231], v[120:121], v[32:33], v[32:33] neg_lo:[0,0,1] neg_hi:[0,0,1]
	v_pk_add_f32 v[116:117], v[116:117], v[222:223]
	v_pk_fma_f32 v[120:121], v[120:121], v[116:117], v[116:117]
	v_rcp_f32_e32 v118, v118
	v_rcp_f32_e32 v119, v119
	v_rcp_f32_e32 v120, v120
	v_rcp_f32_e32 v121, v121
	v_pk_mul_f32 v[204:205], v[228:229], v[118:119]
	v_pk_fma_f32 v[204:205], v[230:231], v[120:121], v[204:205]
	v_pk_fma_f32 v[106:107], v[106:107], v[216:217], v[14:15]
	v_pk_fma_f32 v[110:111], v[110:111], v[218:219], v[18:19]
	v_min_f32_e32 v106, 0x42700000, v106
	v_min_f32_e32 v107, 0x42700000, v107
	v_min_f32_e32 v110, 0x42700000, v110
	v_min_f32_e32 v111, 0x42700000, v111
	v_pk_fma_f32 v[108:109], v[108:109], v[216:217], v[16:17]
	v_pk_fma_f32 v[112:113], v[112:113], v[218:219], v[20:21]
	v_min_f32_e32 v108, 0x42700000, v108
	v_min_f32_e32 v109, 0x42700000, v109
	v_min_f32_e32 v112, 0x42700000, v112
	v_min_f32_e32 v113, 0x42700000, v113
	v_exp_f32_e32 v106, v106
	v_exp_f32_e32 v107, v107
	v_exp_f32_e32 v110, v110
	v_exp_f32_e32 v111, v111
	v_exp_f32_e32 v108, v108
	v_exp_f32_e32 v109, v109
	v_exp_f32_e32 v112, v112
	v_exp_f32_e32 v113, v113
	v_pk_fma_f32 v[228:229], v[106:107], v[10:11], v[10:11] neg_lo:[0,0,1] neg_hi:[0,0,1]
	v_pk_add_f32 v[110:111], v[110:111], v[222:223]
	v_pk_fma_f32 v[106:107], v[106:107], v[110:111], v[110:111]
	v_pk_fma_f32 v[230:231], v[108:109], v[12:13], v[12:13] neg_lo:[0,0,1] neg_hi:[0,0,1]
	v_pk_add_f32 v[112:113], v[112:113], v[222:223]
	v_pk_fma_f32 v[108:109], v[108:109], v[112:113], v[112:113]
	v_rcp_f32_e32 v106, v106
	v_rcp_f32_e32 v107, v107
	v_rcp_f32_e32 v108, v108
	v_rcp_f32_e32 v109, v109
	v_pk_fma_f32 v[204:205], v[228:229], v[106:107], v[204:205]
	v_pk_fma_f32 v[204:205], v[230:231], v[108:109], v[204:205]
	v_pk_fma_f32 v[102:103], v[102:103], v[216:217], v[34:35]
	v_pk_fma_f32 v[98:99], v[98:99], v[218:219], v[38:39]
	v_min_f32_e32 v102, 0x42700000, v102
	v_min_f32_e32 v103, 0x42700000, v103
	v_min_f32_e32 v98, 0x42700000, v98
	v_min_f32_e32 v99, 0x42700000, v99
	v_pk_fma_f32 v[104:105], v[104:105], v[216:217], v[36:37]
	v_pk_fma_f32 v[100:101], v[100:101], v[218:219], v[40:41]
	v_min_f32_e32 v104, 0x42700000, v104
	v_min_f32_e32 v105, 0x42700000, v105
	v_min_f32_e32 v100, 0x42700000, v100
	v_min_f32_e32 v101, 0x42700000, v101
	v_exp_f32_e32 v102, v102
	v_exp_f32_e32 v103, v103
	v_exp_f32_e32 v98, v98
	v_exp_f32_e32 v99, v99
	v_exp_f32_e32 v104, v104
	v_exp_f32_e32 v105, v105
	v_exp_f32_e32 v100, v100
	v_exp_f32_e32 v101, v101
	v_pk_fma_f32 v[228:229], v[102:103], v[30:31], v[30:31] neg_lo:[0,0,1] neg_hi:[0,0,1]
	v_pk_add_f32 v[98:99], v[98:99], v[222:223]
	v_pk_fma_f32 v[102:103], v[102:103], v[98:99], v[98:99]
	v_pk_fma_f32 v[230:231], v[104:105], v[32:33], v[32:33] neg_lo:[0,0,1] neg_hi:[0,0,1]
	v_pk_add_f32 v[100:101], v[100:101], v[222:223]
	v_pk_fma_f32 v[104:105], v[104:105], v[100:101], v[100:101]
	v_rcp_f32_e32 v102, v102
	v_rcp_f32_e32 v103, v103
	v_rcp_f32_e32 v104, v104
	v_rcp_f32_e32 v105, v105
	v_pk_mul_f32 v[206:207], v[228:229], v[102:103]
	v_pk_fma_f32 v[206:207], v[230:231], v[104:105], v[206:207]
	v_pk_fma_f32 v[90:91], v[90:91], v[216:217], v[14:15]
	v_pk_fma_f32 v[94:95], v[94:95], v[218:219], v[18:19]
	v_min_f32_e32 v90, 0x42700000, v90
	v_min_f32_e32 v91, 0x42700000, v91
	v_min_f32_e32 v94, 0x42700000, v94
	v_min_f32_e32 v95, 0x42700000, v95
	v_pk_fma_f32 v[92:93], v[92:93], v[216:217], v[16:17]
	v_pk_fma_f32 v[96:97], v[96:97], v[218:219], v[20:21]
	v_min_f32_e32 v92, 0x42700000, v92
	v_min_f32_e32 v93, 0x42700000, v93
	v_min_f32_e32 v96, 0x42700000, v96
	v_min_f32_e32 v97, 0x42700000, v97
	v_exp_f32_e32 v90, v90
	v_exp_f32_e32 v91, v91
	v_exp_f32_e32 v94, v94
	v_exp_f32_e32 v95, v95
	v_exp_f32_e32 v92, v92
	v_exp_f32_e32 v93, v93
	v_exp_f32_e32 v96, v96
	v_exp_f32_e32 v97, v97
	v_pk_fma_f32 v[228:229], v[90:91], v[10:11], v[10:11] neg_lo:[0,0,1] neg_hi:[0,0,1]
	v_pk_add_f32 v[94:95], v[94:95], v[222:223]
	v_pk_fma_f32 v[90:91], v[90:91], v[94:95], v[94:95]
	v_pk_fma_f32 v[230:231], v[92:93], v[12:13], v[12:13] neg_lo:[0,0,1] neg_hi:[0,0,1]
	v_pk_add_f32 v[96:97], v[96:97], v[222:223]
	v_pk_fma_f32 v[92:93], v[92:93], v[96:97], v[96:97]
	v_rcp_f32_e32 v90, v90
	v_rcp_f32_e32 v91, v91
	v_rcp_f32_e32 v92, v92
	v_rcp_f32_e32 v93, v93
	v_pk_fma_f32 v[206:207], v[228:229], v[90:91], v[206:207]
	v_pk_fma_f32 v[206:207], v[230:231], v[92:93], v[206:207]
	v_pk_fma_f32 v[86:87], v[86:87], v[216:217], v[34:35]
	v_pk_fma_f32 v[82:83], v[82:83], v[218:219], v[38:39]
	v_min_f32_e32 v86, 0x42700000, v86
	v_min_f32_e32 v87, 0x42700000, v87
	v_min_f32_e32 v82, 0x42700000, v82
	v_min_f32_e32 v83, 0x42700000, v83
	v_pk_fma_f32 v[88:89], v[88:89], v[216:217], v[36:37]
	v_pk_fma_f32 v[84:85], v[84:85], v[218:219], v[40:41]
	v_min_f32_e32 v88, 0x42700000, v88
	v_min_f32_e32 v89, 0x42700000, v89
	v_min_f32_e32 v84, 0x42700000, v84
	v_min_f32_e32 v85, 0x42700000, v85
	v_exp_f32_e32 v86, v86
	v_exp_f32_e32 v87, v87
	v_exp_f32_e32 v82, v82
	v_exp_f32_e32 v83, v83
	v_exp_f32_e32 v88, v88
	v_exp_f32_e32 v89, v89
	v_exp_f32_e32 v84, v84
	v_exp_f32_e32 v85, v85
	v_pk_fma_f32 v[228:229], v[86:87], v[30:31], v[30:31] neg_lo:[0,0,1] neg_hi:[0,0,1]
	v_pk_add_f32 v[82:83], v[82:83], v[222:223]
	v_pk_fma_f32 v[86:87], v[86:87], v[82:83], v[82:83]
	v_pk_fma_f32 v[230:231], v[88:89], v[32:33], v[32:33] neg_lo:[0,0,1] neg_hi:[0,0,1]
	v_pk_add_f32 v[84:85], v[84:85], v[222:223]
	v_pk_fma_f32 v[88:89], v[88:89], v[84:85], v[84:85]
	v_rcp_f32_e32 v86, v86
	v_rcp_f32_e32 v87, v87
	v_rcp_f32_e32 v88, v88
	v_rcp_f32_e32 v89, v89
	v_pk_mul_f32 v[208:209], v[228:229], v[86:87]
	v_pk_fma_f32 v[208:209], v[230:231], v[88:89], v[208:209]
	v_pk_fma_f32 v[74:75], v[74:75], v[216:217], v[14:15]
	v_pk_fma_f32 v[78:79], v[78:79], v[218:219], v[18:19]
	v_min_f32_e32 v74, 0x42700000, v74
	v_min_f32_e32 v75, 0x42700000, v75
	v_min_f32_e32 v78, 0x42700000, v78
	v_min_f32_e32 v79, 0x42700000, v79
	v_pk_fma_f32 v[76:77], v[76:77], v[216:217], v[16:17]
	v_pk_fma_f32 v[80:81], v[80:81], v[218:219], v[20:21]
	v_min_f32_e32 v76, 0x42700000, v76
	v_min_f32_e32 v77, 0x42700000, v77
	v_min_f32_e32 v80, 0x42700000, v80
	v_min_f32_e32 v81, 0x42700000, v81
	v_exp_f32_e32 v74, v74
	v_exp_f32_e32 v75, v75
	v_exp_f32_e32 v78, v78
	v_exp_f32_e32 v79, v79
	v_exp_f32_e32 v76, v76
	v_exp_f32_e32 v77, v77
	v_exp_f32_e32 v80, v80
	v_exp_f32_e32 v81, v81
	v_pk_fma_f32 v[228:229], v[74:75], v[10:11], v[10:11] neg_lo:[0,0,1] neg_hi:[0,0,1]
	v_pk_add_f32 v[78:79], v[78:79], v[222:223]
	v_pk_fma_f32 v[74:75], v[74:75], v[78:79], v[78:79]
	v_pk_fma_f32 v[230:231], v[76:77], v[12:13], v[12:13] neg_lo:[0,0,1] neg_hi:[0,0,1]
	v_pk_add_f32 v[80:81], v[80:81], v[222:223]
	v_pk_fma_f32 v[76:77], v[76:77], v[80:81], v[80:81]
	v_rcp_f32_e32 v74, v74
	v_rcp_f32_e32 v75, v75
	v_rcp_f32_e32 v76, v76
	v_rcp_f32_e32 v77, v77
	v_pk_fma_f32 v[208:209], v[228:229], v[74:75], v[208:209]
	v_pk_fma_f32 v[208:209], v[230:231], v[76:77], v[208:209]
	v_pk_fma_f32 v[70:71], v[70:71], v[216:217], v[34:35]
	v_pk_fma_f32 v[66:67], v[66:67], v[218:219], v[38:39]
	v_min_f32_e32 v70, 0x42700000, v70
	v_min_f32_e32 v71, 0x42700000, v71
	v_min_f32_e32 v66, 0x42700000, v66
	v_min_f32_e32 v67, 0x42700000, v67
	v_pk_fma_f32 v[72:73], v[72:73], v[216:217], v[36:37]
	v_pk_fma_f32 v[68:69], v[68:69], v[218:219], v[40:41]
	v_min_f32_e32 v72, 0x42700000, v72
	v_min_f32_e32 v73, 0x42700000, v73
	v_min_f32_e32 v68, 0x42700000, v68
	v_min_f32_e32 v69, 0x42700000, v69
	v_exp_f32_e32 v70, v70
	v_exp_f32_e32 v71, v71
	v_exp_f32_e32 v66, v66
	v_exp_f32_e32 v67, v67
	v_exp_f32_e32 v72, v72
	v_exp_f32_e32 v73, v73
	v_exp_f32_e32 v68, v68
	v_exp_f32_e32 v69, v69
	v_pk_fma_f32 v[228:229], v[70:71], v[30:31], v[30:31] neg_lo:[0,0,1] neg_hi:[0,0,1]
	v_pk_add_f32 v[66:67], v[66:67], v[222:223]
	v_pk_fma_f32 v[70:71], v[70:71], v[66:67], v[66:67]
	v_pk_fma_f32 v[230:231], v[72:73], v[32:33], v[32:33] neg_lo:[0,0,1] neg_hi:[0,0,1]
	v_pk_add_f32 v[68:69], v[68:69], v[222:223]
	v_pk_fma_f32 v[72:73], v[72:73], v[68:69], v[68:69]
	v_rcp_f32_e32 v70, v70
	v_rcp_f32_e32 v71, v71
	v_rcp_f32_e32 v72, v72
	v_rcp_f32_e32 v73, v73
	v_pk_mul_f32 v[210:211], v[228:229], v[70:71]
	v_pk_fma_f32 v[210:211], v[230:231], v[72:73], v[210:211]
	v_pk_fma_f32 v[58:59], v[58:59], v[216:217], v[14:15]
	v_pk_fma_f32 v[62:63], v[62:63], v[218:219], v[18:19]
	v_min_f32_e32 v58, 0x42700000, v58
	v_min_f32_e32 v59, 0x42700000, v59
	v_min_f32_e32 v62, 0x42700000, v62
	v_min_f32_e32 v63, 0x42700000, v63
	v_pk_fma_f32 v[60:61], v[60:61], v[216:217], v[16:17]
	v_pk_fma_f32 v[64:65], v[64:65], v[218:219], v[20:21]
	v_min_f32_e32 v60, 0x42700000, v60
	v_min_f32_e32 v61, 0x42700000, v61
	v_min_f32_e32 v64, 0x42700000, v64
	v_min_f32_e32 v65, 0x42700000, v65
	v_exp_f32_e32 v58, v58
	v_exp_f32_e32 v59, v59
	v_exp_f32_e32 v62, v62
	v_exp_f32_e32 v63, v63
	v_exp_f32_e32 v60, v60
	v_exp_f32_e32 v61, v61
	v_exp_f32_e32 v64, v64
	v_exp_f32_e32 v65, v65
	v_pk_fma_f32 v[228:229], v[58:59], v[10:11], v[10:11] neg_lo:[0,0,1] neg_hi:[0,0,1]
	v_pk_add_f32 v[62:63], v[62:63], v[222:223]
	v_pk_fma_f32 v[58:59], v[58:59], v[62:63], v[62:63]
	v_pk_fma_f32 v[230:231], v[60:61], v[12:13], v[12:13] neg_lo:[0,0,1] neg_hi:[0,0,1]
	v_pk_add_f32 v[64:65], v[64:65], v[222:223]
	v_pk_fma_f32 v[60:61], v[60:61], v[64:65], v[64:65]
	v_rcp_f32_e32 v58, v58
	v_rcp_f32_e32 v59, v59
	v_rcp_f32_e32 v60, v60
	v_rcp_f32_e32 v61, v61
	v_pk_fma_f32 v[210:211], v[228:229], v[58:59], v[210:211]
	v_pk_fma_f32 v[210:211], v[230:231], v[60:61], v[210:211]
	v_pk_fma_f32 v[54:55], v[54:55], v[216:217], v[34:35]
	v_pk_fma_f32 v[50:51], v[50:51], v[218:219], v[38:39]
	v_min_f32_e32 v54, 0x42700000, v54
	v_min_f32_e32 v55, 0x42700000, v55
	v_min_f32_e32 v50, 0x42700000, v50
	v_min_f32_e32 v51, 0x42700000, v51
	v_pk_fma_f32 v[56:57], v[56:57], v[216:217], v[36:37]
	v_pk_fma_f32 v[52:53], v[52:53], v[218:219], v[40:41]
	v_min_f32_e32 v56, 0x42700000, v56
	v_min_f32_e32 v57, 0x42700000, v57
	v_min_f32_e32 v52, 0x42700000, v52
	v_min_f32_e32 v53, 0x42700000, v53
	v_exp_f32_e32 v54, v54
	v_exp_f32_e32 v55, v55
	v_exp_f32_e32 v50, v50
	v_exp_f32_e32 v51, v51
	v_exp_f32_e32 v56, v56
	v_exp_f32_e32 v57, v57
	v_exp_f32_e32 v52, v52
	v_exp_f32_e32 v53, v53
	v_pk_fma_f32 v[228:229], v[54:55], v[30:31], v[30:31] neg_lo:[0,0,1] neg_hi:[0,0,1]
	v_pk_add_f32 v[50:51], v[50:51], v[222:223]
	v_pk_fma_f32 v[54:55], v[54:55], v[50:51], v[50:51]
	v_pk_fma_f32 v[230:231], v[56:57], v[32:33], v[32:33] neg_lo:[0,0,1] neg_hi:[0,0,1]
	v_pk_add_f32 v[52:53], v[52:53], v[222:223]
	v_pk_fma_f32 v[56:57], v[56:57], v[52:53], v[52:53]
	v_rcp_f32_e32 v54, v54
	v_rcp_f32_e32 v55, v55
	v_rcp_f32_e32 v56, v56
	v_rcp_f32_e32 v57, v57
	v_pk_mul_f32 v[212:213], v[228:229], v[54:55]
	v_pk_fma_f32 v[212:213], v[230:231], v[56:57], v[212:213]
	v_pk_fma_f32 v[42:43], v[42:43], v[216:217], v[14:15]
	v_pk_fma_f32 v[46:47], v[46:47], v[218:219], v[18:19]
	v_min_f32_e32 v42, 0x42700000, v42
	v_min_f32_e32 v43, 0x42700000, v43
	v_min_f32_e32 v46, 0x42700000, v46
	v_min_f32_e32 v47, 0x42700000, v47
	v_pk_fma_f32 v[44:45], v[44:45], v[216:217], v[16:17]
	v_pk_fma_f32 v[48:49], v[48:49], v[218:219], v[20:21]
	v_min_f32_e32 v44, 0x42700000, v44
	v_min_f32_e32 v45, 0x42700000, v45
	v_min_f32_e32 v48, 0x42700000, v48
	v_min_f32_e32 v49, 0x42700000, v49
	v_exp_f32_e32 v42, v42
	v_exp_f32_e32 v43, v43
	v_exp_f32_e32 v46, v46
	v_exp_f32_e32 v47, v47
	v_exp_f32_e32 v44, v44
	v_exp_f32_e32 v45, v45
	v_exp_f32_e32 v48, v48
	v_exp_f32_e32 v49, v49
	v_pk_fma_f32 v[228:229], v[42:43], v[10:11], v[10:11] neg_lo:[0,0,1] neg_hi:[0,0,1]
	v_pk_add_f32 v[46:47], v[46:47], v[222:223]
	v_pk_fma_f32 v[42:43], v[42:43], v[46:47], v[46:47]
	v_pk_fma_f32 v[230:231], v[44:45], v[12:13], v[12:13] neg_lo:[0,0,1] neg_hi:[0,0,1]
	v_pk_add_f32 v[48:49], v[48:49], v[222:223]
	v_pk_fma_f32 v[44:45], v[44:45], v[48:49], v[48:49]
	v_rcp_f32_e32 v42, v42
	v_rcp_f32_e32 v43, v43
	v_rcp_f32_e32 v44, v44
	v_rcp_f32_e32 v45, v45
	v_pk_fma_f32 v[212:213], v[228:229], v[42:43], v[212:213]
	v_pk_fma_f32 v[212:213], v[230:231], v[44:45], v[212:213]
	v_pk_fma_f32 v[26:27], v[26:27], v[216:217], v[34:35]
	v_pk_fma_f32 v[22:23], v[22:23], v[218:219], v[38:39]
	v_min_f32_e32 v26, 0x42700000, v26
	v_min_f32_e32 v27, 0x42700000, v27
	v_min_f32_e32 v22, 0x42700000, v22
	v_min_f32_e32 v23, 0x42700000, v23
	v_pk_fma_f32 v[28:29], v[28:29], v[216:217], v[36:37]
	v_pk_fma_f32 v[24:25], v[24:25], v[218:219], v[40:41]
	v_min_f32_e32 v28, 0x42700000, v28
	v_min_f32_e32 v29, 0x42700000, v29
	v_min_f32_e32 v24, 0x42700000, v24
	v_min_f32_e32 v25, 0x42700000, v25
	v_exp_f32_e32 v26, v26
	v_exp_f32_e32 v27, v27
	v_exp_f32_e32 v22, v22
	v_exp_f32_e32 v23, v23
	v_exp_f32_e32 v28, v28
	v_exp_f32_e32 v29, v29
	v_exp_f32_e32 v24, v24
	v_exp_f32_e32 v25, v25
	v_pk_fma_f32 v[228:229], v[26:27], v[30:31], v[30:31] neg_lo:[0,0,1] neg_hi:[0,0,1]
	v_pk_add_f32 v[22:23], v[22:23], v[222:223]
	v_pk_fma_f32 v[26:27], v[26:27], v[22:23], v[22:23]
	v_pk_fma_f32 v[230:231], v[28:29], v[32:33], v[32:33] neg_lo:[0,0,1] neg_hi:[0,0,1]
	v_pk_add_f32 v[24:25], v[24:25], v[222:223]
	v_pk_fma_f32 v[28:29], v[28:29], v[24:25], v[24:25]
	v_rcp_f32_e32 v26, v26
	v_rcp_f32_e32 v27, v27
	v_rcp_f32_e32 v28, v28
	v_rcp_f32_e32 v29, v29
	v_pk_mul_f32 v[214:215], v[228:229], v[26:27]
	v_pk_fma_f32 v[214:215], v[230:231], v[28:29], v[214:215]
	v_pk_fma_f32 v[2:3], v[2:3], v[216:217], v[14:15]
	v_pk_fma_f32 v[6:7], v[6:7], v[218:219], v[18:19]
	v_min_f32_e32 v2, 0x42700000, v2
	v_min_f32_e32 v3, 0x42700000, v3
	v_min_f32_e32 v6, 0x42700000, v6
	v_min_f32_e32 v7, 0x42700000, v7
	v_pk_fma_f32 v[4:5], v[4:5], v[216:217], v[16:17]
	v_pk_fma_f32 v[8:9], v[8:9], v[218:219], v[20:21]
	v_min_f32_e32 v4, 0x42700000, v4
	v_min_f32_e32 v5, 0x42700000, v5
	v_min_f32_e32 v8, 0x42700000, v8
	v_min_f32_e32 v9, 0x42700000, v9
	v_exp_f32_e32 v2, v2
	v_exp_f32_e32 v3, v3
	v_exp_f32_e32 v6, v6
	v_exp_f32_e32 v7, v7
	v_exp_f32_e32 v4, v4
	v_exp_f32_e32 v5, v5
	v_exp_f32_e32 v8, v8
	v_exp_f32_e32 v9, v9
	v_pk_fma_f32 v[228:229], v[2:3], v[10:11], v[10:11] neg_lo:[0,0,1] neg_hi:[0,0,1]
	v_pk_add_f32 v[6:7], v[6:7], v[222:223]
	v_pk_fma_f32 v[2:3], v[2:3], v[6:7], v[6:7]
	v_pk_fma_f32 v[230:231], v[4:5], v[12:13], v[12:13] neg_lo:[0,0,1] neg_hi:[0,0,1]
	v_pk_add_f32 v[8:9], v[8:9], v[222:223]
	v_pk_fma_f32 v[4:5], v[4:5], v[8:9], v[8:9]
	v_rcp_f32_e32 v2, v2
	v_rcp_f32_e32 v3, v3
	v_rcp_f32_e32 v4, v4
	v_rcp_f32_e32 v5, v5
	v_pk_fma_f32 v[214:215], v[228:229], v[2:3], v[214:215]
	v_pk_fma_f32 v[214:215], v[230:231], v[4:5], v[214:215]
	v_add_f32_e32 v240, v200, v201
	v_add_f32_e32 v241, v202, v203
	v_add_f32_e32 v242, v204, v205
	v_add_f32_e32 v243, v206, v207
	v_add_f32_e32 v244, v208, v209
	v_add_f32_e32 v245, v210, v211
	v_add_f32_e32 v246, v212, v213
	v_add_f32_e32 v247, v214, v215
	ds_bpermute_b32 v200, v181, v240
	ds_bpermute_b32 v201, v181, v241
	ds_bpermute_b32 v202, v181, v242
	ds_bpermute_b32 v203, v181, v243
	ds_bpermute_b32 v204, v181, v244
	ds_bpermute_b32 v205, v181, v245
	ds_bpermute_b32 v206, v181, v246
	ds_bpermute_b32 v207, v181, v247
	s_waitcnt lgkmcnt(0)
	v_add_f32_e32 v240, v240, v200
	v_add_f32_e32 v241, v241, v201
	v_add_f32_e32 v242, v242, v202
	v_add_f32_e32 v243, v243, v203
	v_add_f32_e32 v244, v244, v204
	v_add_f32_e32 v245, v245, v205
	v_add_f32_e32 v246, v246, v206
	v_add_f32_e32 v247, v247, v207
	ds_bpermute_b32 v200, v183, v240
	ds_bpermute_b32 v201, v183, v241
	ds_bpermute_b32 v202, v183, v242
	ds_bpermute_b32 v203, v183, v243
	ds_bpermute_b32 v204, v183, v244
	ds_bpermute_b32 v205, v183, v245
	ds_bpermute_b32 v206, v183, v246
	ds_bpermute_b32 v207, v183, v247
	s_waitcnt lgkmcnt(0)
	v_add_f32_e32 v240, v240, v200
	v_add_f32_e32 v241, v241, v201
	v_add_f32_e32 v242, v242, v202
	v_add_f32_e32 v243, v243, v203
	v_add_f32_e32 v244, v244, v204
	v_add_f32_e32 v245, v245, v205
	v_add_f32_e32 v246, v246, v206
	v_add_f32_e32 v247, v247, v207
	s_and_saveexec_b64 s[64:65], vcc
	ds_write2_b32 v232, v240, v241 offset0:0 offset1:16
	ds_write2_b32 v232, v242, v243 offset0:32 offset1:48
	ds_write2_b32 v232, v244, v245 offset0:64 offset1:80
	ds_write2_b32 v232, v246, v247 offset0:96 offset1:112
	s_mov_b64 exec, s[64:65]
	v_mov_b32_e32 v4, 0
	v_lshlrev_b32_e32 v10, 2, v189
	v_mov_b32_e32 v11, v4
	v_and_b32_e32 v70, 0x1c0, v0
	s_waitcnt lgkmcnt(0)
	v_lshl_add_u64 v[2:3], s[44:45], 0, v[10:11]
	s_lshl_b64 s[0:1], s[42:43], 17
	v_lshlrev_b32_e32 v6, 8, v70
	v_mov_b32_e32 v7, v4
	v_lshl_add_u64 v[2:3], v[2:3], 0, s[0:1]
	v_lshl_add_u64 v[2:3], v[2:3], 0, v[6:7]
	s_movk_i32 s0, 0x1000
	v_add_co_u32_e32 v6, vcc, s0, v2
	s_movk_i32 s0, 0x2000
	s_nop 0
	v_addc_co_u32_e32 v7, vcc, 0, v3, vcc
	v_add_co_u32_e32 v8, vcc, s0, v2
	s_movk_i32 s0, 0x3000
	s_nop 0
	v_addc_co_u32_e32 v9, vcc, 0, v3, vcc
	global_load_dword v78, v[2:3], off
	global_load_dword v77, v[2:3], off offset:256
	global_load_dword v76, v[2:3], off offset:512
	global_load_dword v75, v[2:3], off offset:768
	global_load_dword v74, v[2:3], off offset:1024
	global_load_dword v73, v[2:3], off offset:1280
	global_load_dword v72, v[2:3], off offset:1536
	global_load_dword v71, v[2:3], off offset:1792
	global_load_dword v69, v[2:3], off offset:2048
	global_load_dword v65, v[2:3], off offset:2304
	global_load_dword v63, v[2:3], off offset:2560
	global_load_dword v62, v[2:3], off offset:2816
	global_load_dword v61, v[2:3], off offset:3072
	global_load_dword v51, v[2:3], off offset:3328
	global_load_dword v52, v[2:3], off offset:3584
	global_load_dword v53, v[2:3], off offset:3840
	v_add_co_u32_e32 v2, vcc, s0, v2
	global_load_dword v55, v[6:7], off offset:256
	global_load_dword v56, v[6:7], off offset:512
	global_load_dword v57, v[6:7], off offset:768
	global_load_dword v54, v[6:7], off offset:1024
	global_load_dword v48, v[6:7], off offset:1280
	global_load_dword v49, v[6:7], off offset:1536
	global_load_dword v50, v[6:7], off offset:1792
	global_load_dword v47, v[6:7], off offset:2048
	global_load_dword v43, v[8:9], off
	global_load_dword v44, v[8:9], off offset:256
	global_load_dword v45, v[8:9], off offset:512
	global_load_dword v46, v[8:9], off offset:768
	global_load_dword v42, v[8:9], off offset:1024
	global_load_dword v39, v[8:9], off offset:1280
	global_load_dword v40, v[8:9], off offset:1536
	global_load_dword v41, v[8:9], off offset:1792
	global_load_dword v33, v[8:9], off offset:2048
	global_load_dword v34, v[8:9], off offset:2304
	global_load_dword v35, v[8:9], off offset:2560
	global_load_dword v36, v[8:9], off offset:2816
	global_load_dword v32, v[8:9], off offset:3072
	global_load_dword v24, v[8:9], off offset:3328
	global_load_dword v25, v[8:9], off offset:3584
	global_load_dword v26, v[8:9], off offset:3840
	v_addc_co_u32_e32 v3, vcc, 0, v3, vcc
	global_load_dword v66, v[6:7], off offset:2304
	global_load_dword v67, v[6:7], off offset:2560
	global_load_dword v68, v[6:7], off offset:2816
	global_load_dword v64, v[6:7], off offset:3072
	global_load_dword v58, v[6:7], off offset:3328
	global_load_dword v59, v[6:7], off offset:3584
	global_load_dword v60, v[6:7], off offset:3840
	global_load_dword v28, v[2:3], off
	global_load_dword v29, v[2:3], off offset:256
	global_load_dword v30, v[2:3], off offset:512
	global_load_dword v31, v[2:3], off offset:768
	global_load_dword v27, v[2:3], off offset:1024
	global_load_dword v21, v[2:3], off offset:1280
	global_load_dword v22, v[2:3], off offset:1536
	global_load_dword v23, v[2:3], off offset:1792
	global_load_dword v16, v[2:3], off offset:2048
	global_load_dword v79, v[8:9], off offset:-4096
	global_load_dword v18, v[2:3], off offset:2304
	global_load_dword v19, v[2:3], off offset:2560
	global_load_dword v20, v[2:3], off offset:2816
	global_load_dword v17, v[2:3], off offset:3072
	global_load_dword v15, v[2:3], off offset:3328
	global_load_dword v13, v[2:3], off offset:3584
	global_load_dword v11, v[2:3], off offset:3840
	v_lshl_add_u32 v2, v189, 2, 0
	v_add_u32_e32 v5, 0x20000, v2
	s_waitcnt vmcnt(63) expcnt(7) lgkmcnt(15)
	s_barrier
	ds_read2st64_b32 v[2:3], v5 offset1:1
	ds_read2st64_b32 v[6:7], v5 offset0:2 offset1:3
	ds_read2st64_b32 v[8:9], v5 offset0:4 offset1:5
	ds_read2st64_b32 v[80:81], v5 offset0:6 offset1:7
	s_mov_b32 s7, 0
	s_waitcnt lgkmcnt(3)
	v_add_f32_e32 v2, s2, v2
	v_add_f32_e32 v3, s2, v3
	s_waitcnt lgkmcnt(2)
	v_add_f32_e32 v2, v2, v6
	v_add_f32_e32 v3, v3, v7
	s_waitcnt lgkmcnt(1)
	v_add_f32_e32 v2, v2, v8
	v_add_f32_e32 v6, v3, v9
	s_waitcnt lgkmcnt(0)
	v_add_f32_e32 v12, v2, v80
	ds_read2st64_b32 v[2:3], v5 offset0:8 offset1:9
	v_add_f32_e32 v14, v6, v81
	ds_read2st64_b32 v[6:7], v5 offset0:10 offset1:11
	ds_read2st64_b32 v[8:9], v5 offset0:12 offset1:13
	ds_read2st64_b32 v[80:81], v5 offset0:14 offset1:15
	v_cmp_gt_u32_e64 s[0:1], 64, v0
	s_waitcnt lgkmcnt(3)
	v_add_f32_e32 v2, v12, v2
	v_add_f32_e32 v3, v14, v3
	s_waitcnt lgkmcnt(2)
	v_add_f32_e32 v2, v2, v6
	v_add_f32_e32 v3, v3, v7
	s_waitcnt lgkmcnt(1)
	v_add_f32_e32 v2, v2, v8
	v_add_f32_e32 v3, v3, v9
	s_waitcnt lgkmcnt(0)
	v_add_f32_e32 v2, v2, v80
	v_add_f32_e32 v3, v3, v81
	v_max_f32_e32 v5, v2, v3
	ds_bpermute_b32 v6, v183, v5
	s_waitcnt lgkmcnt(0)
	v_max_f32_e32 v6, v6, v6
	v_max_f32_e32 v5, v5, v6
	ds_bpermute_b32 v6, v181, v5
	s_waitcnt lgkmcnt(0)
	v_max_f32_e32 v6, v6, v6
	v_max_f32_e32 v5, v5, v6
	ds_bpermute_b32 v6, v1, v5
	s_waitcnt lgkmcnt(0)
	v_max_f32_e32 v6, v6, v6
	v_max_f32_e32 v5, v5, v6
	ds_bpermute_b32 v6, v180, v5
	s_waitcnt lgkmcnt(0)
	v_max_f32_e32 v6, v6, v6
	v_max_f32_e32 v5, v5, v6
	ds_bpermute_b32 v6, v182, v5
	s_waitcnt lgkmcnt(0)
	v_max_f32_e32 v6, v6, v6
	v_max_f32_e32 v5, v5, v6
	ds_bpermute_b32 v6, v184, v5
	s_waitcnt lgkmcnt(0)
	v_max_f32_e32 v6, v6, v6
	v_max_f32_e32 v14, v5, v6
	v_sub_f32_e32 v2, v2, v14
	v_sub_f32_e32 v3, v3, v14
	v_mul_f32_e32 v2, 0x3fb8aa3b, v2
	v_mul_f32_e32 v3, 0x3fb8aa3b, v3
	v_exp_f32_e32 v2, v2
	v_exp_f32_e32 v3, v3
	s_nop 0
	v_add_f32_e32 v5, v2, v3
	ds_bpermute_b32 v6, v183, v5
	s_waitcnt lgkmcnt(0)
	v_add_f32_e32 v5, v5, v6
	ds_bpermute_b32 v6, v181, v5
	s_waitcnt lgkmcnt(0)
	v_add_f32_e32 v5, v5, v6
	ds_bpermute_b32 v6, v1, v5
	s_waitcnt lgkmcnt(0)
	v_add_f32_e32 v5, v5, v6
	ds_bpermute_b32 v6, v180, v5
	s_waitcnt lgkmcnt(0)
	v_add_f32_e32 v5, v5, v6
	ds_bpermute_b32 v6, v182, v5
	s_waitcnt lgkmcnt(0)
	v_add_f32_e32 v37, v5, v6
	ds_bpermute_b32 v38, v184, v37
	s_and_saveexec_b64 s[2:3], s[0:1]
	s_cbranch_execz .LBB5_166
	s_add_i32 s12, 0, 0x21000
	v_lshl_add_u32 v5, v189, 2, s12
	v_lshl_add_u32 v6, v0, 2, s12
	ds_write_b32 v5, v2
	ds_write_b32 v6, v3 offset:256

	.amdhsa_kernel _Z8k_expertPKDF16_S0_PKfPcPiS0_S2_S2_S2_S2_PfS5_S4_S2_S2_S2_S2_S5_S2_S2_S2_
		.amdhsa_group_segment_fixed_size 0
		.amdhsa_private_segment_fixed_size 0
		.amdhsa_kernarg_size 168
		.amdhsa_user_sgpr_count 2
		.amdhsa_user_sgpr_dispatch_ptr 0
		.amdhsa_user_sgpr_queue_ptr 0
		.amdhsa_user_sgpr_kernarg_segment_ptr 1
		.amdhsa_user_sgpr_dispatch_id 0
		.amdhsa_user_sgpr_kernarg_preload_length 0
		.amdhsa_user_sgpr_kernarg_preload_offset 0
		.amdhsa_user_sgpr_private_segment_size 0
		.amdhsa_uses_dynamic_stack 0
		.amdhsa_enable_private_segment 0
		.amdhsa_system_sgpr_workgroup_id_x 1
		.amdhsa_system_sgpr_workgroup_id_y 0
		.amdhsa_system_sgpr_workgroup_id_z 0
		.amdhsa_system_sgpr_workgroup_info 0
		.amdhsa_system_vgpr_workitem_id 0
		.amdhsa_next_free_vgpr 256
		.amdhsa_next_free_sgpr 96
		.amdhsa_accum_offset 256
		.amdhsa_reserve_vcc 1
		.amdhsa_float_round_mode_32 0
		.amdhsa_float_round_mode_16_64 0
		.amdhsa_float_denorm_mode_32 3
		.amdhsa_float_denorm_mode_16_64 3
		.amdhsa_dx10_clamp 1
		.amdhsa_ieee_mode 1
		.amdhsa_fp16_overflow 0
		.amdhsa_tg_split 0
		.amdhsa_exception_fp_ieee_invalid_op 0
		.amdhsa_exception_fp_denorm_src 0
		.amdhsa_exception_fp_ieee_div_zero 0
		.amdhsa_exception_fp_ieee_overflow 0
		.amdhsa_exception_fp_ieee_underflow 0
		.amdhsa_exception_fp_ieee_inexact 0
		.amdhsa_exception_int_div_zero 0
	.end_amdhsa_kernel

amdhsa.kernels:
  - .agpr_count:     0
    .args:
      - .actual_access:  read_only
        .address_space:  global
        .offset:         0
        .size:           8
        .value_kind:     global_buffer
      - .actual_access:  read_only
        .address_space:  global
        .offset:         8
        .size:           8
        .value_kind:     global_buffer
      - .actual_access:  read_only
        .address_space:  global
        .offset:         16
        .size:           8
        .value_kind:     global_buffer
      - .actual_access:  write_only
        .address_space:  global
        .offset:         24
        .size:           8
        .value_kind:     global_buffer
      - .actual_access:  write_only
        .address_space:  global
        .offset:         32
        .size:           8
        .value_kind:     global_buffer
      - .actual_access:  read_only
        .address_space:  global
        .offset:         40
        .size:           8
        .value_kind:     global_buffer
      - .actual_access:  read_only
        .address_space:  global
        .offset:         48
        .size:           8
        .value_kind:     global_buffer
      - .actual_access:  read_only
        .address_space:  global
        .offset:         56
        .size:           8
        .value_kind:     global_buffer
      - .actual_access:  read_only
        .address_space:  global
        .offset:         64
        .size:           8
        .value_kind:     global_buffer
      - .actual_access:  read_only
        .address_space:  global
        .offset:         72
        .size:           8
        .value_kind:     global_buffer
      - .actual_access:  read_only
        .address_space:  global
        .offset:         80
        .size:           8
        .value_kind:     global_buffer
    .group_segment_fixed_size: 16384
    .kernarg_segment_align: 8
    .kernarg_segment_size: 88
    .language:       OpenCL C
    .language_version:
      - 2
      - 0
    .max_flat_workgroup_size: 768
    .name:           _Z9k_router2PKfPKDF16_S0_PDF16_PfPiS0_S0_S4_S5_S4_
    .private_segment_fixed_size: 0
    .sgpr_count:     21
    .sgpr_spill_count: 0
    .symbol:         _Z9k_router2PKfPKDF16_S0_PDF16_PfPiS0_S0_S4_S5_S4_.kd
    .uniform_work_group_size: 1
    .uses_dynamic_stack: false
    .vgpr_count:     168
    .vgpr_spill_count: 0
    .wavefront_size: 64
  - .agpr_count:     0
    .args:
      - .actual_access:  read_only
        .address_space:  global
        .offset:         0
        .size:           8
        .value_kind:     global_buffer
      - .actual_access:  read_only
        .address_space:  global
        .offset:         8
        .size:           8
        .value_kind:     global_buffer
      - .actual_access:  read_only
        .address_space:  global
        .offset:         16
        .size:           8
        .value_kind:     global_buffer
      - .actual_access:  write_only
        .address_space:  global
        .offset:         24
        .size:           8
        .value_kind:     global_buffer
      - .actual_access:  write_only
        .address_space:  global
        .offset:         32
        .size:           8
        .value_kind:     global_buffer
      - .actual_access:  write_only
        .address_space:  global
        .offset:         40
        .size:           8
        .value_kind:     global_buffer
    .group_segment_fixed_size: 256
    .kernarg_segment_align: 8
    .kernarg_segment_size: 48
    .language:       OpenCL C
    .language_version:
      - 2
      - 0
    .max_flat_workgroup_size: 256
    .name:           _Z6k_gatePKfS0_S0_PfPiS1_
    .private_segment_fixed_size: 0
    .sgpr_count:     26
    .sgpr_spill_count: 0
    .symbol:         _Z6k_gatePKfS0_S0_PfPiS1_.kd
    .uniform_work_group_size: 1
    .uses_dynamic_stack: false
    .vgpr_count:     51
    .vgpr_spill_count: 0
    .wavefront_size: 64
  - .agpr_count:     0
    .args:
      - .actual_access:  read_only
        .address_space:  global
        .offset:         0
        .size:           8
        .value_kind:     global_buffer
      - .actual_access:  write_only
        .address_space:  global
        .offset:         8
        .size:           8
        .value_kind:     global_buffer
      - .actual_access:  read_only
        .address_space:  global
        .offset:         16
        .size:           8
        .value_kind:     global_buffer
      - .actual_access:  read_only
        .address_space:  global
        .offset:         24
        .size:           8
        .value_kind:     global_buffer
      - .actual_access:  read_only
        .address_space:  global
        .offset:         32
        .size:           8
        .value_kind:     global_buffer
      - .actual_access:  write_only
        .address_space:  global
        .offset:         40
        .size:           8
        .value_kind:     global_buffer
      - .actual_access:  write_only
        .address_space:  global
        .offset:         48
        .size:           8
        .value_kind:     global_buffer
      - .actual_access:  write_only
        .address_space:  global
        .offset:         56
        .size:           8
        .value_kind:     global_buffer
      - .actual_access:  write_only
        .address_space:  global
        .offset:         64
        .size:           8
        .value_kind:     global_buffer
      - .actual_access:  write_only
        .address_space:  global
        .offset:         72
        .size:           8
        .value_kind:     global_buffer
    .group_segment_fixed_size: 16640
    .kernarg_segment_align: 8
    .kernarg_segment_size: 80
    .language:       OpenCL C
    .language_version:
      - 2
      - 0
    .max_flat_workgroup_size: 256
    .name:           _Z10k_prep_allPKfPDF16_S0_S0_S0_S1_S1_PiS2_S2_
    .private_segment_fixed_size: 0
    .sgpr_count:     20
    .sgpr_spill_count: 0
    .symbol:         _Z10k_prep_allPKfPDF16_S0_S0_S0_S1_S1_PiS2_S2_.kd
    .uniform_work_group_size: 1
    .uses_dynamic_stack: false
    .vgpr_count:     37
    .vgpr_spill_count: 0
    .wavefront_size: 64
  - .agpr_count:     0
    .args:
      - .address_space:  global
        .offset:         0
        .size:           8
        .value_kind:     global_buffer
      - .address_space:  global
        .offset:         8
        .size:           8
        .value_kind:     global_buffer
      - .actual_access:  read_only
        .address_space:  global
        .offset:         16
        .size:           8
        .value_kind:     global_buffer
      - .actual_access:  read_only
        .address_space:  global
        .offset:         24
        .size:           8
        .value_kind:     global_buffer
      - .actual_access:  write_only
        .address_space:  global
        .offset:         32
        .size:           8
        .value_kind:     global_buffer
    .group_segment_fixed_size: 0
    .kernarg_segment_align: 8
    .kernarg_segment_size: 40
    .language:       OpenCL C
    .language_version:
      - 2
      - 0
    .max_flat_workgroup_size: 512
    .name:           _Z7k_gemm1PKDF16_S0_PKfPKiPDF16_
    .private_segment_fixed_size: 0
    .sgpr_count:     36
    .sgpr_spill_count: 0
    .symbol:         _Z7k_gemm1PKDF16_S0_PKfPKiPDF16_.kd
    .uniform_work_group_size: 1
    .uses_dynamic_stack: false
    .vgpr_count:     240
    .vgpr_spill_count: 0
    .wavefront_size: 64
  - .agpr_count:     0
    .args:
      - .address_space:  global
        .offset:         0
        .size:           8
        .value_kind:     global_buffer
      - .actual_access:  read_only
        .address_space:  global
        .offset:         8
        .size:           8
        .value_kind:     global_buffer
      - .actual_access:  read_only
        .address_space:  global
        .offset:         16
        .size:           8
        .value_kind:     global_buffer
      - .actual_access:  read_only
        .address_space:  global
        .offset:         24
        .size:           8
        .value_kind:     global_buffer
      - .actual_access:  read_only
        .address_space:  global
        .offset:         32
        .size:           8
        .value_kind:     global_buffer
      - .actual_access:  read_only
        .address_space:  global
        .offset:         40
        .size:           8
        .value_kind:     global_buffer
      - .actual_access:  read_only
        .address_space:  global
        .offset:         48
        .size:           8
        .value_kind:     global_buffer
      - .actual_access:  write_only
        .address_space:  global
        .offset:         56
        .size:           8
        .value_kind:     global_buffer
      - .actual_access:  write_only
        .address_space:  global
        .offset:         64
        .size:           8
        .value_kind:     global_buffer
    .group_segment_fixed_size: 0
    .kernarg_segment_align: 8
    .kernarg_segment_size: 72
    .language:       OpenCL C
    .language_version:
      - 2
      - 0
    .max_flat_workgroup_size: 512
    .name:           _Z11k_gemm2poolPKDF16_S0_PKfS2_S2_S2_PKiPfS5_
    .private_segment_fixed_size: 0
    .sgpr_count:     32
    .sgpr_spill_count: 0
    .symbol:         _Z11k_gemm2poolPKDF16_S0_PKfS2_S2_S2_PKiPfS5_.kd
    .uniform_work_group_size: 1
    .uses_dynamic_stack: false
    .vgpr_count:     198
    .vgpr_spill_count: 0
    .wavefront_size: 64
  - .agpr_count:     0
    .args:
      - .address_space:  global
        .offset:         0
        .size:           8
        .value_kind:     global_buffer
      - .address_space:  global
        .offset:         8
        .size:           8
        .value_kind:     global_buffer
      - .actual_access:  read_only
        .address_space:  global
        .offset:         16
        .size:           8
        .value_kind:     global_buffer
      - .address_space:  global
        .offset:         24
        .size:           8
        .value_kind:     global_buffer
      - .address_space:  global
        .offset:         32
        .size:           8
        .value_kind:     global_buffer
      - .actual_access:  read_only
        .address_space:  global
        .offset:         40
        .size:           8
        .value_kind:     global_buffer
      - .actual_access:  read_only
        .address_space:  global
        .offset:         48
        .size:           8
        .value_kind:     global_buffer
      - .actual_access:  read_only
        .address_space:  global
        .offset:         56
        .size:           8
        .value_kind:     global_buffer
      - .actual_access:  read_only
        .address_space:  global
        .offset:         64
        .size:           8
        .value_kind:     global_buffer
      - .actual_access:  read_only
        .address_space:  global
        .offset:         72
        .size:           8
        .value_kind:     global_buffer
      - .address_space:  global
        .offset:         80
        .size:           8
        .value_kind:     global_buffer
      - .address_space:  global
        .offset:         88
        .size:           8
        .value_kind:     global_buffer
      - .address_space:  global
        .offset:         96
        .size:           8
        .value_kind:     global_buffer
      - .actual_access:  read_only
        .address_space:  global
        .offset:         104
        .size:           8
        .value_kind:     global_buffer
      - .actual_access:  read_only
        .address_space:  global
        .offset:         112
        .size:           8
        .value_kind:     global_buffer
      - .actual_access:  read_only
        .address_space:  global
        .offset:         120
        .size:           8
        .value_kind:     global_buffer
      - .actual_access:  read_only
        .address_space:  global
        .offset:         128
        .size:           8
        .value_kind:     global_buffer
      - .actual_access:  write_only
        .address_space:  global
        .offset:         136
        .size:           8
        .value_kind:     global_buffer
      - .actual_access:  read_only
        .address_space:  global
        .offset:         144
        .size:           8
        .value_kind:     global_buffer
      - .actual_access:  read_only
        .address_space:  global
        .offset:         152
        .size:           8
        .value_kind:     global_buffer
      - .actual_access:  read_only
        .address_space:  global
        .offset:         160
        .size:           8
        .value_kind:     global_buffer
    .group_segment_fixed_size: 0
    .kernarg_segment_align: 8
    .kernarg_segment_size: 168
    .language:       OpenCL C
    .language_version:
      - 2
      - 0
    .max_flat_workgroup_size: 512
    .name:           _Z8k_expertPKDF16_S0_PKfPcPiS0_S2_S2_S2_S2_PfS5_S4_S2_S2_S2_S2_S5_S2_S2_S2_
    .private_segment_fixed_size: 0
    .sgpr_count:     102
    .sgpr_spill_count: 0
    .symbol:         _Z8k_expertPKDF16_S0_PKfPcPiS0_S2_S2_S2_S2_PfS5_S4_S2_S2_S2_S2_S5_S2_S2_S2_.kd
    .uniform_work_group_size: 1
    .uses_dynamic_stack: false
    .vgpr_count:     256
    .vgpr_spill_count: 0
    .wavefront_size: 64
  - .agpr_count:     0
    .args:
      - .actual_access:  read_only
        .address_space:  global
        .offset:         0
        .size:           8
        .value_kind:     global_buffer
      - .actual_access:  read_only
        .address_space:  global
        .offset:         8
        .size:           8
        .value_kind:     global_buffer
      - .actual_access:  read_only
        .address_space:  global
        .offset:         16
        .size:           8
        .value_kind:     global_buffer
      - .actual_access:  read_only
        .address_space:  global
        .offset:         24
        .size:           8
        .value_kind:     global_buffer
      - .actual_access:  read_only
        .address_space:  global
        .offset:         32
        .size:           8
        .value_kind:     global_buffer
      - .actual_access:  read_only
        .address_space:  global
        .offset:         40
        .size:           8
        .value_kind:     global_buffer
      - .actual_access:  read_only
        .address_space:  global
        .offset:         48
        .size:           8
        .value_kind:     global_buffer
      - .actual_access:  read_only
        .address_space:  global
        .offset:         56
        .size:           8
        .value_kind:     global_buffer
      - .actual_access:  write_only
        .address_space:  global
        .offset:         64
        .size:           8
        .value_kind:     global_buffer
    .group_segment_fixed_size: 8768
    .kernarg_segment_align: 8
    .kernarg_segment_size: 72
    .language:       OpenCL C
    .language_version:
      - 2
      - 0
    .max_flat_workgroup_size: 1024
    .name:           _Z7k_finalPKfS0_S0_S0_S0_PKiS0_S0_Pf
    .private_segment_fixed_size: 0
    .sgpr_count:     24
    .sgpr_spill_count: 0
    .symbol:         _Z7k_finalPKfS0_S0_S0_S0_PKiS0_S0_Pf.kd
    .uniform_work_group_size: 1
    .uses_dynamic_stack: false
    .vgpr_count:     83
    .vgpr_spill_count: 0
    .wavefront_size: 64
